# speedup vs baseline: 1.0487x; 1.0102x over previous
_Z6k_prepPKiS0_PiS1_S1_S1_S1_S1_S1_PKfPKDF16_PDF16_Pf:
	s_cmpk_lt_u32 s2, 521
	s_cbranch_scc1 .Lp1_entry
	s_cmpk_lt_u32 s2, 912
	s_cbranch_scc1 .Lp2_entry
	s_cmpk_lt_u32 s2, 2475
	s_cbranch_scc1 .Lpx_entry
	s_endpgm
.Lpx_entry:
	v_and_b32_e32 v50, 63, v0
	s_load_dwordx2 s[4:5], s[0:1], 0x50
	v_lshlrev_b32_e32 v1, 4, v0
	v_or_b32_e32 v18, 0x80, v0
	v_lshlrev_b32_e32 v10, 4, v18
	v_or_b32_e32 v20, 0x180, v0
	s_waitcnt lgkmcnt(0)
	global_load_dwordx4 v[2:5], v1, s[4:5]
	global_load_dwordx4 v[6:9], v10, s[4:5]
	v_or_b32_e32 v1, 0x100, v0
	v_lshlrev_b32_e32 v19, 4, v1
	v_lshlrev_b32_e32 v21, 4, v20
	global_load_dwordx4 v[10:13], v19, s[4:5]
	global_load_dwordx4 v[14:17], v21, s[4:5]
	v_lshrrev_b32_e32 v19, 4, v0
	s_sub_i32 s8, s2, 912
	s_lshl_b32 s8, s8, 1
	v_lshrrev_b32_e32 v23, 6, v0
	s_movk_i32 s4, 0x70
	s_movk_i32 s5, 0xf0
	v_mov_b32_e32 v21, 0x80
	s_movk_i32 s6, 0x170
	s_movk_i32 s7, 0x1f0
	v_mov_b32_e32 v22, 0x180
	v_bitop3_b32 v19, v19, 15, v0 bitop3:0x48
	v_lshrrev_b32_e32 v18, 4, v18
	v_lshrrev_b32_e32 v20, 4, v20
	v_or_b32_e32 v23, s8, v23
	s_mov_b32 s3, 0xc350
	v_bitop3_b32 v21, v0, s5, v21 bitop3:0xc8
	v_bitop3_b32 v22, v0, s7, v22 bitop3:0xc8
	v_and_or_b32 v24, v0, s4, v19
	v_xor_b32_e32 v18, v18, v0
	v_and_or_b32 v19, v1, s6, v19
	v_xor_b32_e32 v20, v20, v0
	v_lshlrev_b32_e32 v1, 4, v23
	v_lshlrev_b32_e32 v23, 4, v24
	v_and_or_b32 v18, v18, 15, v21
	v_and_or_b32 v20, v20, 15, v22
	v_cmp_gt_i32_e32 vcc, s3, v1
	v_lshlrev_b32_e32 v19, 4, v19
	v_lshlrev_b32_e32 v18, 4, v18
	v_lshlrev_b32_e32 v20, 4, v20
	s_waitcnt vmcnt(3)
	ds_write_b128 v23, v[2:5]
	s_waitcnt vmcnt(2)
	ds_write_b128 v18, v[6:9]
	s_waitcnt vmcnt(1)
	ds_write_b128 v19, v[10:13]
	s_waitcnt vmcnt(0)
	ds_write_b128 v20, v[14:17]
	s_waitcnt lgkmcnt(0)
	s_barrier
	s_and_saveexec_b64 s[6:7], vcc
	s_cbranch_execz .LBB1_12
	v_and_b32_e32 v51, 15, v0
	s_load_dwordx2 s[4:5], s[0:1], 0x48
	v_or_b32_e32 v46, v1, v51
	v_mov_b32_e32 v2, 0xc34f
	v_cmp_gt_i32_e32 vcc, s3, v46
	v_lshrrev_b32_e32 v1, 4, v50
	v_lshlrev_b32_e32 v42, 5, v1
	v_cndmask_b32_e32 v2, v2, v46, vcc
	v_ashrrev_i32_e32 v3, 31, v2
	v_lshlrev_b64 v[2:3], 9, v[2:3]
	s_waitcnt lgkmcnt(0)
	v_lshl_add_u64 v[2:3], s[4:5], 0, v[2:3]
	v_mov_b32_e32 v43, 0
	v_lshl_add_u64 v[30:31], v[2:3], 0, v[42:43]
	global_load_dwordx4 v[26:29], v[30:31], off offset:16 nt
	global_load_dwordx4 v[34:37], v[30:31], off nt
	global_load_dwordx4 v[18:21], v[30:31], off offset:144 nt
	global_load_dwordx4 v[22:25], v[30:31], off offset:128 nt
	global_load_dwordx4 v[10:13], v[30:31], off offset:272 nt
	global_load_dwordx4 v[14:17], v[30:31], off offset:256 nt
	global_load_dwordx4 v[2:5], v[30:31], off offset:400 nt
	global_load_dwordx4 v[6:9], v[30:31], off offset:384 nt
	s_load_dwordx2 s[4:5], s[0:1], 0x58
	v_bitop3_b32 v30, v1, v0, 15 bitop3:0x78
	v_lshlrev_b32_e32 v31, 8, v51
	v_lshl_or_b32 v38, v30, 4, v31
	ds_read_b128 v[30:33], v38
	ds_read_b128 v[38:41], v38 offset:4096
	v_ashrrev_i32_e32 v47, 31, v46
	v_lshlrev_b64 v[44:45], 8, v[46:47]
	s_waitcnt lgkmcnt(0)
	v_lshl_add_u64 v[44:45], s[4:5], 0, v[44:45]
	v_and_b32_e32 v42, 48, v50
	v_lshlrev_b32_e32 v52, 7, v51
	v_lshl_add_u64 v[48:49], v[44:45], 0, v[42:43]
	s_waitcnt vmcnt(7)
	v_cvt_pk_f16_f32 v44, v26, v27
	s_waitcnt vmcnt(6)
	v_cvt_f16_f32_e32 v54, v34
	v_cvt_f16_f32_e32 v53, v35
	v_cvt_pk_f16_f32 v42, v34, v35
	v_cvt_pk_f16_f32 v43, v36, v37
	v_cvt_pk_f16_f32 v45, v28, v29
	s_and_saveexec_b64 s[4:5], vcc
	s_cbranch_execz .LBB1_4
	global_store_dwordx4 v[48:49], v[42:45], off

.Lp1_entry:
	s_load_dwordx4 s[4:7], s[0:1], 0x0
	s_load_dwordx2 s[8:9], s[0:1], 0x20
	s_load_dwordx2 s[10:11], s[0:1], 0x28
	s_load_dwordx2 s[12:13], s[0:1], 0x50
	v_lshlrev_b32_e32 v1, 4, v0
	v_mov_b32_e32 v2, 0
	v_mov_b32_e32 v3, 0
	v_mov_b32_e32 v4, 0
	v_mov_b32_e32 v5, 0
	ds_write_b128 v1, v[2:5]
	s_mul_i32 s3, s2, 0x180
	v_add_u32_e32 v4, s3, v0
	v_add_u32_e32 v5, 0x80, v4
	v_add_u32_e32 v6, 0x100, v4
	s_mov_b32 s14, 0x30d40
	v_cmp_gt_u32_e64 s[16:17], s14, v4
	v_cmp_gt_u32_e64 s[18:19], s14, v5
	v_cmp_gt_u32_e64 s[20:21], s14, v6
	v_min_u32_e32 v4, 0x30d3f, v4
	v_min_u32_e32 v5, 0x30d3f, v5
	v_min_u32_e32 v6, 0x30d3f, v6
	v_lshlrev_b32_e32 v4, 4, v4
	v_lshlrev_b32_e32 v5, 4, v5
	v_lshlrev_b32_e32 v6, 4, v6
	s_waitcnt lgkmcnt(0)
	s_add_u32 s14, s4, 0x30d400
	s_addc_u32 s15, s5, 0
	global_load_dwordx4 v[8:11], v4, s[6:7] nt
	global_load_dwordx4 v[12:15], v4, s[4:5] nt
	global_load_dwordx4 v[16:19], v4, s[14:15] nt
	global_load_dwordx4 v[20:23], v5, s[6:7] nt
	global_load_dwordx4 v[24:27], v5, s[4:5] nt
	global_load_dwordx4 v[28:31], v5, s[14:15] nt
	global_load_dwordx4 v[32:35], v6, s[6:7] nt
	global_load_dwordx4 v[36:39], v6, s[4:5] nt
	global_load_dwordx4 v[40:43], v6, s[14:15] nt
	v_mov_b32_e32 v48, 1
	s_mov_b32 s31, 0
	s_mov_b32 s30, 0xc350
	s_barrier
	s_waitcnt vmcnt(6)
	v_mul_lo_u32 v44, v12, v8
	v_mul_lo_u32 v45, v16, v8
	v_cmp_ne_u32_e64 s[22:23], 0, v8
	v_max_u32_e32 v46, v44, v45
	v_cmp_gt_u32_e32 vcc, s30, v46
	s_and_b64 vcc, vcc, s[22:23]
	s_and_b64 vcc, vcc, s[16:17]
	s_andn2_b64 s[24:25], s[16:17], s[22:23]
	s_bcnt1_i32_b64 s26, s[24:25]
	s_add_i32 s31, s31, s26
	v_lshl_or_b32 v12, v45, 16, v44
	v_cndmask_b32_e32 v12, -1, v12, vcc
	v_lshrrev_b32_e32 v47, 21, v12
	v_and_b32_e32 v47, 0x7fc, v47
	ds_add_rtn_u32 v16, v47, v48
	v_mul_lo_u32 v44, v13, v9
	v_mul_lo_u32 v45, v17, v9
	v_cmp_ne_u32_e64 s[22:23], 0, v9
	v_max_u32_e32 v46, v44, v45
	v_cmp_gt_u32_e32 vcc, s30, v46
	s_and_b64 vcc, vcc, s[22:23]
	s_and_b64 vcc, vcc, s[16:17]
	s_andn2_b64 s[24:25], s[16:17], s[22:23]
	s_bcnt1_i32_b64 s26, s[24:25]
	s_add_i32 s31, s31, s26
	v_lshl_or_b32 v13, v45, 16, v44
	v_cndmask_b32_e32 v13, -1, v13, vcc
	v_lshrrev_b32_e32 v47, 21, v13
	v_and_b32_e32 v47, 0x7fc, v47
	ds_add_rtn_u32 v17, v47, v48
	v_mul_lo_u32 v44, v14, v10
	v_mul_lo_u32 v45, v18, v10
	v_cmp_ne_u32_e64 s[22:23], 0, v10
	v_max_u32_e32 v46, v44, v45
	v_cmp_gt_u32_e32 vcc, s30, v46
	s_and_b64 vcc, vcc, s[22:23]
	s_and_b64 vcc, vcc, s[16:17]
	s_andn2_b64 s[24:25], s[16:17], s[22:23]
	s_bcnt1_i32_b64 s26, s[24:25]
	s_add_i32 s31, s31, s26
	v_lshl_or_b32 v14, v45, 16, v44
	v_cndmask_b32_e32 v14, -1, v14, vcc
	v_lshrrev_b32_e32 v47, 21, v14
	v_and_b32_e32 v47, 0x7fc, v47
	ds_add_rtn_u32 v18, v47, v48
	v_mul_lo_u32 v44, v15, v11
	v_mul_lo_u32 v45, v19, v11
	v_cmp_ne_u32_e64 s[22:23], 0, v11
	v_max_u32_e32 v46, v44, v45
	v_cmp_gt_u32_e32 vcc, s30, v46
	s_and_b64 vcc, vcc, s[22:23]
	s_and_b64 vcc, vcc, s[16:17]
	s_andn2_b64 s[24:25], s[16:17], s[22:23]
	s_bcnt1_i32_b64 s26, s[24:25]
	s_add_i32 s31, s31, s26
	v_lshl_or_b32 v15, v45, 16, v44
	v_cndmask_b32_e32 v15, -1, v15, vcc
	v_lshrrev_b32_e32 v47, 21, v15
	v_and_b32_e32 v47, 0x7fc, v47
	ds_add_rtn_u32 v19, v47, v48
	s_waitcnt vmcnt(3)
	v_mul_lo_u32 v44, v24, v20
	v_mul_lo_u32 v45, v28, v20
	v_cmp_ne_u32_e64 s[22:23], 0, v20
	v_max_u32_e32 v46, v44, v45
	v_cmp_gt_u32_e32 vcc, s30, v46
	s_and_b64 vcc, vcc, s[22:23]
	s_and_b64 vcc, vcc, s[18:19]
	s_andn2_b64 s[24:25], s[18:19], s[22:23]
	s_bcnt1_i32_b64 s26, s[24:25]
	s_add_i32 s31, s31, s26
	v_lshl_or_b32 v24, v45, 16, v44
	v_cndmask_b32_e32 v24, -1, v24, vcc
	v_lshrrev_b32_e32 v47, 21, v24
	v_and_b32_e32 v47, 0x7fc, v47
	ds_add_rtn_u32 v28, v47, v48
	v_mul_lo_u32 v44, v25, v21
	v_mul_lo_u32 v45, v29, v21
	v_cmp_ne_u32_e64 s[22:23], 0, v21
	v_max_u32_e32 v46, v44, v45
	v_cmp_gt_u32_e32 vcc, s30, v46
	s_and_b64 vcc, vcc, s[22:23]
	s_and_b64 vcc, vcc, s[18:19]
	s_andn2_b64 s[24:25], s[18:19], s[22:23]
	s_bcnt1_i32_b64 s26, s[24:25]
	s_add_i32 s31, s31, s26
	v_lshl_or_b32 v25, v45, 16, v44
	v_cndmask_b32_e32 v25, -1, v25, vcc
	v_lshrrev_b32_e32 v47, 21, v25
	v_and_b32_e32 v47, 0x7fc, v47
	ds_add_rtn_u32 v29, v47, v48
	v_mul_lo_u32 v44, v26, v22
	v_mul_lo_u32 v45, v30, v22
	v_cmp_ne_u32_e64 s[22:23], 0, v22
	v_max_u32_e32 v46, v44, v45
	v_cmp_gt_u32_e32 vcc, s30, v46
	s_and_b64 vcc, vcc, s[22:23]
	s_and_b64 vcc, vcc, s[18:19]
	s_andn2_b64 s[24:25], s[18:19], s[22:23]
	s_bcnt1_i32_b64 s26, s[24:25]
	s_add_i32 s31, s31, s26
	v_lshl_or_b32 v26, v45, 16, v44
	v_cndmask_b32_e32 v26, -1, v26, vcc
	v_lshrrev_b32_e32 v47, 21, v26
	v_and_b32_e32 v47, 0x7fc, v47
	ds_add_rtn_u32 v30, v47, v48
	v_mul_lo_u32 v44, v27, v23
	v_mul_lo_u32 v45, v31, v23
	v_cmp_ne_u32_e64 s[22:23], 0, v23
	v_max_u32_e32 v46, v44, v45
	v_cmp_gt_u32_e32 vcc, s30, v46
	s_and_b64 vcc, vcc, s[22:23]
	s_and_b64 vcc, vcc, s[18:19]
	s_andn2_b64 s[24:25], s[18:19], s[22:23]
	s_bcnt1_i32_b64 s26, s[24:25]
	s_add_i32 s31, s31, s26
	v_lshl_or_b32 v27, v45, 16, v44
	v_cndmask_b32_e32 v27, -1, v27, vcc
	v_lshrrev_b32_e32 v47, 21, v27
	v_and_b32_e32 v47, 0x7fc, v47
	ds_add_rtn_u32 v31, v47, v48
	s_waitcnt vmcnt(0)
	v_mul_lo_u32 v44, v36, v32
	v_mul_lo_u32 v45, v40, v32
	v_cmp_ne_u32_e64 s[22:23], 0, v32
	v_max_u32_e32 v46, v44, v45
	v_cmp_gt_u32_e32 vcc, s30, v46
	s_and_b64 vcc, vcc, s[22:23]
	s_and_b64 vcc, vcc, s[20:21]
	s_andn2_b64 s[24:25], s[20:21], s[22:23]
	s_bcnt1_i32_b64 s26, s[24:25]
	s_add_i32 s31, s31, s26
	v_lshl_or_b32 v36, v45, 16, v44
	v_cndmask_b32_e32 v36, -1, v36, vcc
	v_lshrrev_b32_e32 v47, 21, v36
	v_and_b32_e32 v47, 0x7fc, v47
	ds_add_rtn_u32 v40, v47, v48
	v_mul_lo_u32 v44, v37, v33
	v_mul_lo_u32 v45, v41, v33
	v_cmp_ne_u32_e64 s[22:23], 0, v33
	v_max_u32_e32 v46, v44, v45
	v_cmp_gt_u32_e32 vcc, s30, v46
	s_and_b64 vcc, vcc, s[22:23]
	s_and_b64 vcc, vcc, s[20:21]
	s_andn2_b64 s[24:25], s[20:21], s[22:23]
	s_bcnt1_i32_b64 s26, s[24:25]
	s_add_i32 s31, s31, s26
	v_lshl_or_b32 v37, v45, 16, v44
	v_cndmask_b32_e32 v37, -1, v37, vcc
	v_lshrrev_b32_e32 v47, 21, v37
	v_and_b32_e32 v47, 0x7fc, v47
	ds_add_rtn_u32 v41, v47, v48
	v_mul_lo_u32 v44, v38, v34
	v_mul_lo_u32 v45, v42, v34
	v_cmp_ne_u32_e64 s[22:23], 0, v34
	v_max_u32_e32 v46, v44, v45
	v_cmp_gt_u32_e32 vcc, s30, v46
	s_and_b64 vcc, vcc, s[22:23]
	s_and_b64 vcc, vcc, s[20:21]
	s_andn2_b64 s[24:25], s[20:21], s[22:23]
	s_bcnt1_i32_b64 s26, s[24:25]
	s_add_i32 s31, s31, s26
	v_lshl_or_b32 v38, v45, 16, v44
	v_cndmask_b32_e32 v38, -1, v38, vcc
	v_lshrrev_b32_e32 v47, 21, v38
	v_and_b32_e32 v47, 0x7fc, v47
	ds_add_rtn_u32 v42, v47, v48
	v_mul_lo_u32 v44, v39, v35
	v_mul_lo_u32 v45, v43, v35
	v_cmp_ne_u32_e64 s[22:23], 0, v35
	v_max_u32_e32 v46, v44, v45
	v_cmp_gt_u32_e32 vcc, s30, v46
	s_and_b64 vcc, vcc, s[22:23]
	s_and_b64 vcc, vcc, s[20:21]
	s_andn2_b64 s[24:25], s[20:21], s[22:23]
	s_bcnt1_i32_b64 s26, s[24:25]
	s_add_i32 s31, s31, s26
	v_lshl_or_b32 v39, v45, 16, v44
	v_cndmask_b32_e32 v39, -1, v39, vcc
	v_lshrrev_b32_e32 v47, 21, v39
	v_and_b32_e32 v47, 0x7fc, v47
	ds_add_rtn_u32 v43, v47, v48
	s_waitcnt lgkmcnt(0)
	s_barrier
	v_readfirstlane_b32 s3, v0
	s_cmp_lt_u32 s3, 64
	s_cbranch_scc0 .Lp1_scan_done
	v_lshlrev_b32_e32 v1, 5, v0
	ds_read_b128 v[8:11], v1 offset:0
	ds_read_b128 v[20:23], v1 offset:16
	v_mov_b32_e32 v44, 0
	s_waitcnt lgkmcnt(0)
	v_mov_b32_e32 v54, v44
	v_add_u32_e32 v44, v44, v8
	v_mov_b32_e32 v55, v44
	v_add_u32_e32 v44, v44, v9
	v_mov_b32_e32 v56, v44
	v_add_u32_e32 v44, v44, v10
	v_mov_b32_e32 v57, v44
	v_add_u32_e32 v44, v44, v11
	v_mov_b32_e32 v58, v44
	v_add_u32_e32 v44, v44, v20
	v_mov_b32_e32 v59, v44
	v_add_u32_e32 v44, v44, v21
	v_mov_b32_e32 v60, v44
	v_add_u32_e32 v44, v44, v22
	v_mov_b32_e32 v61, v44
	v_add_u32_e32 v44, v44, v23
	v_mov_b32_e32 v45, v44
	s_nop 1
	v_add_u32_dpp v45, v45, v45 row_shr:1 row_mask:0xf bank_mask:0xf bound_ctrl:1
	s_nop 1
	v_add_u32_dpp v45, v45, v45 row_shr:2 row_mask:0xf bank_mask:0xf bound_ctrl:1
	s_nop 1
	v_add_u32_dpp v45, v45, v45 row_shr:4 row_mask:0xf bank_mask:0xf bound_ctrl:1
	s_nop 1
	v_add_u32_dpp v45, v45, v45 row_shr:8 row_mask:0xf bank_mask:0xf bound_ctrl:1
	s_nop 1
	v_add_u32_dpp v45, v45, v45 row_bcast:15 row_mask:0xa bank_mask:0xf
	s_nop 1
	v_add_u32_dpp v45, v45, v45 row_bcast:31 row_mask:0xc bank_mask:0xf
	s_nop 1
	v_sub_u32_e32 v46, v45, v44
	v_add_u32_e32 v54, v54, v46
	v_add_u32_e32 v55, v55, v46
	v_add_u32_e32 v56, v56, v46
	v_add_u32_e32 v57, v57, v46
	v_add_u32_e32 v58, v58, v46
	v_add_u32_e32 v59, v59, v46
	v_add_u32_e32 v60, v60, v46
	v_add_u32_e32 v61, v61, v46
	ds_write_b128 v1, v[54:57] offset:0
	ds_write_b128 v1, v[58:61] offset:16
	v_lshl_or_b32 v8, v8, 16, v54
	v_lshl_or_b32 v9, v9, 16, v55
	v_lshl_or_b32 v10, v10, 16, v56
	v_lshl_or_b32 v11, v11, 16, v57
	v_lshl_or_b32 v20, v20, 16, v58
	v_lshl_or_b32 v21, v21, 16, v59
	v_lshl_or_b32 v22, v22, 16, v60
	v_lshl_or_b32 v23, v23, 16, v61
	s_lshl_b32 s3, s2, 11
	s_add_u32 s24, s12, 0x41a000
	s_addc_u32 s25, s13, 0
	s_add_u32 s24, s24, s3
	s_addc_u32 s25, s25, 0
	global_store_dwordx4 v1, v[8:11], s[24:25] offset:0 sc1
	global_store_dwordx4 v1, v[20:23], s[24:25] offset:16 sc1
.Lp1_scan_done:
	s_waitcnt lgkmcnt(0)
	s_barrier
	v_lshrrev_b32_e32 v8, 21, v12
	v_and_b32_e32 v8, 0x7fc, v8
	v_lshrrev_b32_e32 v9, 21, v13
	v_and_b32_e32 v9, 0x7fc, v9
	v_lshrrev_b32_e32 v10, 21, v14
	v_and_b32_e32 v10, 0x7fc, v10
	v_lshrrev_b32_e32 v11, 21, v15
	v_and_b32_e32 v11, 0x7fc, v11
	v_lshrrev_b32_e32 v20, 21, v24
	v_and_b32_e32 v20, 0x7fc, v20
	v_lshrrev_b32_e32 v21, 21, v25
	v_and_b32_e32 v21, 0x7fc, v21
	v_lshrrev_b32_e32 v22, 21, v26
	v_and_b32_e32 v22, 0x7fc, v22
	v_lshrrev_b32_e32 v23, 21, v27
	v_and_b32_e32 v23, 0x7fc, v23
	v_lshrrev_b32_e32 v32, 21, v36
	v_and_b32_e32 v32, 0x7fc, v32
	v_lshrrev_b32_e32 v33, 21, v37
	v_and_b32_e32 v33, 0x7fc, v33
	v_lshrrev_b32_e32 v34, 21, v38
	v_and_b32_e32 v34, 0x7fc, v34
	v_lshrrev_b32_e32 v35, 21, v39
	v_and_b32_e32 v35, 0x7fc, v35
	ds_read_b32 v8, v8
	ds_read_b32 v9, v9
	ds_read_b32 v10, v10
	ds_read_b32 v11, v11
	ds_read_b32 v20, v20
	ds_read_b32 v21, v21
	ds_read_b32 v22, v22
	ds_read_b32 v23, v23
	ds_read_b32 v32, v32
	ds_read_b32 v33, v33
	ds_read_b32 v34, v34
	ds_read_b32 v35, v35
	s_waitcnt lgkmcnt(0)
	v_add_lshl_u32 v8, v8, v16, 2
	ds_write_b32 v8, v12 offset:2048
	v_add_lshl_u32 v9, v9, v17, 2
	ds_write_b32 v9, v13 offset:2048
	v_add_lshl_u32 v10, v10, v18, 2
	ds_write_b32 v10, v14 offset:2048
	v_add_lshl_u32 v11, v11, v19, 2
	ds_write_b32 v11, v15 offset:2048
	v_add_lshl_u32 v20, v20, v28, 2
	ds_write_b32 v20, v24 offset:2048
	v_add_lshl_u32 v21, v21, v29, 2
	ds_write_b32 v21, v25 offset:2048
	v_add_lshl_u32 v22, v22, v30, 2
	ds_write_b32 v22, v26 offset:2048
	v_add_lshl_u32 v23, v23, v31, 2
	ds_write_b32 v23, v27 offset:2048
	v_add_lshl_u32 v32, v32, v40, 2
	ds_write_b32 v32, v36 offset:2048
	v_add_lshl_u32 v33, v33, v41, 2
	ds_write_b32 v33, v37 offset:2048
	v_add_lshl_u32 v34, v34, v42, 2
	ds_write_b32 v34, v38 offset:2048
	v_add_lshl_u32 v35, v35, v43, 2
	ds_write_b32 v35, v39 offset:2048
	s_waitcnt lgkmcnt(0)
	s_barrier
	v_lshlrev_b32_e32 v1, 4, v0
	ds_read_b128 v[8:11], v1 offset:2048
	ds_read_b128 v[12:15], v1 offset:4096
	ds_read_b128 v[16:19], v1 offset:6144
	s_mul_i32 s3, s2, 0x1800
	s_add_u32 s26, s12, 0x1a000
	s_addc_u32 s27, s13, 0
	s_add_u32 s26, s26, s3
	s_addc_u32 s27, s27, 0
	v_add_u32_e32 v2, 0x1000, v1
	s_waitcnt lgkmcnt(2)
	global_store_dwordx4 v1, v[8:11], s[26:27] sc1
	s_waitcnt lgkmcnt(1)
	global_store_dwordx4 v1, v[12:15], s[26:27] offset:2048 sc1
	s_waitcnt lgkmcnt(0)
	global_store_dwordx4 v2, v[16:19], s[26:27] sc1
	s_waitcnt vmcnt(0)
	s_barrier
	v_and_b32_e32 v1, 63, v0
	v_cmp_eq_u32_e32 vcc, 0, v1
	s_and_saveexec_b64 s[22:23], vcc
	s_cbranch_execz .Lp1_end
	s_cmp_eq_u32 s31, 0
	s_cbranch_scc1 .Lp1_nomask
	s_and_b32 s3, s2, 63
	s_lshl_b32 s3, s3, 6
	v_mov_b32_e32 v2, s31
	v_mov_b32_e32 v3, s3
	global_atomic_add v3, v2, s[8:9]
.Lp1_nomask:
	v_cmp_eq_u32_e32 vcc, 0, v0
	s_and_b64 exec, exec, vcc
	s_cbranch_execz .Lp1_end
	v_mov_b32_e32 v2, 1
	s_and_b32 s3, s2, 63
	s_cmp_lt_u32 s3, 9
	s_cselect_b32 s24, 8, 7
	s_lshl_b32 s3, s3, 6
	s_add_u32 s3, s3, 8
	v_mov_b32_e32 v3, s3
	global_atomic_add v4, v3, v2, s[8:9] sc0
	s_waitcnt vmcnt(0)
	v_readfirstlane_b32 s3, v4
	s_cmp_lg_u32 s3, s24
	s_cbranch_scc1 .Lp1_end
	v_mov_b32_e32 v3, 4
	global_atomic_add v3, v2, s[8:9] offset:0
	global_atomic_add v3, v2, s[8:9] offset:64
	global_atomic_add v3, v2, s[8:9] offset:128
	global_atomic_add v3, v2, s[8:9] offset:192
	global_atomic_add v3, v2, s[8:9] offset:256
	global_atomic_add v3, v2, s[8:9] offset:320
	global_atomic_add v3, v2, s[8:9] offset:384
	global_atomic_add v3, v2, s[8:9] offset:448
	global_atomic_add v3, v2, s[8:9] offset:512
	global_atomic_add v3, v2, s[8:9] offset:576
	global_atomic_add v3, v2, s[8:9] offset:640
	global_atomic_add v3, v2, s[8:9] offset:704
	global_atomic_add v3, v2, s[8:9] offset:768
	global_atomic_add v3, v2, s[8:9] offset:832
	global_atomic_add v3, v2, s[8:9] offset:896
	global_atomic_add v3, v2, s[8:9] offset:960

.Lp2_entry:
	s_load_dwordx2 s[4:5], s[0:1], 0x10
	s_load_dwordx2 s[6:7], s[0:1], 0x18
	s_load_dwordx2 s[10:11], s[0:1], 0x28
	s_load_dwordx4 s[16:19], s[0:1], 0x30
	s_load_dwordx2 s[20:21], s[0:1], 0x40
	s_load_dwordx2 s[12:13], s[0:1], 0x50
	s_load_dwordx2 s[8:9], s[0:1], 0x20
	s_sub_i32 s33, s2, 521
	s_mov_b32 s30, 0xc350
	v_lshlrev_b32_e32 v1, 3, v0
	v_mov_b32_e32 v2, 0
	v_mov_b32_e32 v3, 0
	ds_write_b64 v1, v[2:3]
	ds_write_b64 v1, v[2:3] offset:1024
	ds_write_b64 v1, v[2:3] offset:2048
	v_mov_b32_e32 v12, 1
	v_mov_b32_e32 v19, 0
	s_mov_b64 s[38:39], 0
	v_mov_b32_e32 v18, 0x400
	s_waitcnt lgkmcnt(0)
	s_lshl_b32 s35, s33, 2
	s_add_u32 s24, s12, 0x41a000
	s_addc_u32 s25, s13, 0
	s_add_u32 s24, s24, s35
	s_addc_u32 s25, s25, 0
	s_add_u32 s26, s12, 0x1a000
	s_addc_u32 s27, s13, 0
	v_readfirstlane_b32 s3, v0
	s_cmp_lt_u32 s3, 64
	s_cbranch_scc0 .Lp2_polled
	s_mov_b32 s34, 0
	s_mov_b64 s[22:23], exec
	s_mov_b64 exec, 1
	s_and_b32 s3, s33, 15
	s_lshl_b32 s3, s3, 6
	s_add_u32 s3, s3, 4
	v_mov_b32_e32 v17, s3

.Lp2_polled:
	s_barrier
	v_lshlrev_b32_e32 v13, 11, v0
	global_load_dword v2, v13, s[24:25] sc1
	v_add_u32_e32 v14, 0x40000, v13
	global_load_dword v3, v14, s[24:25] sc1
	v_add_u32_e32 v14, 0x80000, v13
	global_load_dword v4, v14, s[24:25] sc1
	v_add_u32_e32 v14, 0xc0000, v13
	global_load_dword v5, v14, s[24:25] sc1
	v_add_u32_e32 v14, 0x100000, v13
	v_mov_b32_e32 v6, 0
	v_cmp_gt_u32_e32 vcc, 9, v0
	s_and_saveexec_b64 s[22:23], vcc
	global_load_dword v6, v14, s[24:25] sc1
	s_mov_b64 exec, s[22:23]
	v_mul_u32_u24_e32 v13, 0x1800, v0
	s_waitcnt vmcnt(0)
	v_lshrrev_b32_e32 v7, 16, v2
	v_and_b32_e32 v2, 0xffff, v2
	v_lshl_add_u32 v2, v2, 2, v13
	v_lshrrev_b32_e32 v8, 16, v3
	v_and_b32_e32 v3, 0xffff, v3
	v_add_u32_e32 v14, 0xc0000, v13
	v_lshl_add_u32 v3, v3, 2, v14
	v_lshrrev_b32_e32 v9, 16, v4
	v_and_b32_e32 v4, 0xffff, v4
	v_add_u32_e32 v14, 0x180000, v13
	v_lshl_add_u32 v4, v4, 2, v14
	v_lshrrev_b32_e32 v10, 16, v5
	v_and_b32_e32 v5, 0xffff, v5
	v_add_u32_e32 v14, 0x240000, v13
	v_lshl_add_u32 v5, v5, 2, v14
	v_lshrrev_b32_e32 v11, 16, v6
	v_and_b32_e32 v6, 0xffff, v6
	v_add_u32_e32 v14, 0x300000, v13
	v_lshl_add_u32 v6, v6, 2, v14
	v_cmp_lt_u32_e32 vcc, 0, v7
	s_and_saveexec_b64 s[22:23], vcc
	global_load_dwordx4 v[20:23], v2, s[26:27] sc1
	v_cmp_lt_u32_e32 vcc, 4, v7
	s_and_b64 exec, exec, vcc
	global_load_dwordx4 v[24:27], v2, s[26:27] offset:16 sc1
	s_mov_b64 exec, s[22:23]
	v_cmp_lt_u32_e32 vcc, 0, v8
	s_and_saveexec_b64 s[22:23], vcc
	global_load_dwordx4 v[28:31], v3, s[26:27] sc1
	v_cmp_lt_u32_e32 vcc, 4, v8
	s_and_b64 exec, exec, vcc
	global_load_dwordx4 v[32:35], v3, s[26:27] offset:16 sc1
	s_mov_b64 exec, s[22:23]
	v_cmp_lt_u32_e32 vcc, 0, v9
	s_and_saveexec_b64 s[22:23], vcc
	global_load_dwordx4 v[36:39], v4, s[26:27] sc1
	v_cmp_lt_u32_e32 vcc, 4, v9
	s_and_b64 exec, exec, vcc
	global_load_dwordx4 v[40:43], v4, s[26:27] offset:16 sc1
	s_mov_b64 exec, s[22:23]
	v_cmp_lt_u32_e32 vcc, 0, v10
	s_and_saveexec_b64 s[22:23], vcc
	global_load_dwordx4 v[44:47], v5, s[26:27] sc1
	v_cmp_lt_u32_e32 vcc, 4, v10
	s_and_b64 exec, exec, vcc
	global_load_dwordx4 v[48:51], v5, s[26:27] offset:16 sc1
	s_mov_b64 exec, s[22:23]
	v_cmp_lt_u32_e32 vcc, 0, v11
	s_and_saveexec_b64 s[22:23], vcc
	global_load_dwordx4 v[52:55], v6, s[26:27] sc1
	v_cmp_lt_u32_e32 vcc, 4, v11
	s_and_b64 exec, exec, vcc
	global_load_dwordx4 v[56:59], v6, s[26:27] offset:16 sc1
	s_mov_b64 exec, s[22:23]
	s_waitcnt vmcnt(0)
	v_cmp_lt_u32_e32 vcc, 0, v7
	s_cbranch_vccz .Lp2_c0_p1done
	s_and_saveexec_b64 s[22:23], vcc
	v_bfe_u32 v13, v20, 16, 7
	v_lshlrev_b32_e32 v13, 2, v13
	ds_add_rtn_u32 v60, v13, v12
	s_mov_b64 exec, s[22:23]
	v_cmp_lt_u32_e32 vcc, 1, v7
	s_cbranch_vccz .Lp2_c0_p1done
	s_and_saveexec_b64 s[22:23], vcc
	v_bfe_u32 v13, v21, 16, 7
	v_lshlrev_b32_e32 v13, 2, v13
	ds_add_rtn_u32 v61, v13, v12
	s_mov_b64 exec, s[22:23]
	v_cmp_lt_u32_e32 vcc, 2, v7
	s_cbranch_vccz .Lp2_c0_p1done
	s_and_saveexec_b64 s[22:23], vcc
	v_bfe_u32 v13, v22, 16, 7
	v_lshlrev_b32_e32 v13, 2, v13
	ds_add_rtn_u32 v62, v13, v12
	s_mov_b64 exec, s[22:23]
	v_cmp_lt_u32_e32 vcc, 3, v7
	s_cbranch_vccz .Lp2_c0_p1done
	s_and_saveexec_b64 s[22:23], vcc
	v_bfe_u32 v13, v23, 16, 7
	v_lshlrev_b32_e32 v13, 2, v13
	ds_add_rtn_u32 v63, v13, v12
	s_mov_b64 exec, s[22:23]
	v_cmp_lt_u32_e32 vcc, 4, v7
	s_cbranch_vccz .Lp2_c0_p1done
	s_and_saveexec_b64 s[22:23], vcc
	v_bfe_u32 v13, v24, 16, 7
	v_lshlrev_b32_e32 v13, 2, v13
	ds_add_rtn_u32 v64, v13, v12
	s_mov_b64 exec, s[22:23]
	v_cmp_lt_u32_e32 vcc, 5, v7
	s_cbranch_vccz .Lp2_c0_p1done
	s_and_saveexec_b64 s[22:23], vcc
	v_bfe_u32 v13, v25, 16, 7
	v_lshlrev_b32_e32 v13, 2, v13
	ds_add_rtn_u32 v65, v13, v12
	s_mov_b64 exec, s[22:23]
	v_cmp_lt_u32_e32 vcc, 6, v7
	s_cbranch_vccz .Lp2_c0_p1done
	s_and_saveexec_b64 s[22:23], vcc
	v_bfe_u32 v13, v26, 16, 7
	v_lshlrev_b32_e32 v13, 2, v13
	ds_add_rtn_u32 v66, v13, v12
	s_mov_b64 exec, s[22:23]
	v_cmp_lt_u32_e32 vcc, 7, v7
	s_cbranch_vccz .Lp2_c0_p1done
	s_and_saveexec_b64 s[22:23], vcc
	v_bfe_u32 v13, v27, 16, 7
	v_lshlrev_b32_e32 v13, 2, v13
	ds_add_rtn_u32 v67, v13, v12
	s_mov_b64 exec, s[22:23]
.Lp2_c0_p1done:
	s_waitcnt lgkmcnt(7)
	v_cmp_lt_u32_e32 vcc, 0, v8
	s_cbranch_vccz .Lp2_c1_p1done
	s_and_saveexec_b64 s[22:23], vcc
	v_bfe_u32 v13, v28, 16, 7
	v_lshlrev_b32_e32 v13, 2, v13
	ds_add_rtn_u32 v68, v13, v12
	s_mov_b64 exec, s[22:23]
	v_cmp_lt_u32_e32 vcc, 1, v8
	s_cbranch_vccz .Lp2_c1_p1done
	s_and_saveexec_b64 s[22:23], vcc
	v_bfe_u32 v13, v29, 16, 7
	v_lshlrev_b32_e32 v13, 2, v13
	ds_add_rtn_u32 v69, v13, v12
	s_mov_b64 exec, s[22:23]
	v_cmp_lt_u32_e32 vcc, 2, v8
	s_cbranch_vccz .Lp2_c1_p1done
	s_and_saveexec_b64 s[22:23], vcc
	v_bfe_u32 v13, v30, 16, 7
	v_lshlrev_b32_e32 v13, 2, v13
	ds_add_rtn_u32 v70, v13, v12
	s_mov_b64 exec, s[22:23]
	v_cmp_lt_u32_e32 vcc, 3, v8
	s_cbranch_vccz .Lp2_c1_p1done
	s_and_saveexec_b64 s[22:23], vcc
	v_bfe_u32 v13, v31, 16, 7
	v_lshlrev_b32_e32 v13, 2, v13
	ds_add_rtn_u32 v71, v13, v12
	s_mov_b64 exec, s[22:23]
	v_cmp_lt_u32_e32 vcc, 4, v8
	s_cbranch_vccz .Lp2_c1_p1done
	s_and_saveexec_b64 s[22:23], vcc
	v_bfe_u32 v13, v32, 16, 7
	v_lshlrev_b32_e32 v13, 2, v13
	ds_add_rtn_u32 v72, v13, v12
	s_mov_b64 exec, s[22:23]
	v_cmp_lt_u32_e32 vcc, 5, v8
	s_cbranch_vccz .Lp2_c1_p1done
	s_and_saveexec_b64 s[22:23], vcc
	v_bfe_u32 v13, v33, 16, 7
	v_lshlrev_b32_e32 v13, 2, v13
	ds_add_rtn_u32 v73, v13, v12
	s_mov_b64 exec, s[22:23]
	v_cmp_lt_u32_e32 vcc, 6, v8
	s_cbranch_vccz .Lp2_c1_p1done
	s_and_saveexec_b64 s[22:23], vcc
	v_bfe_u32 v13, v34, 16, 7
	v_lshlrev_b32_e32 v13, 2, v13
	ds_add_rtn_u32 v74, v13, v12
	s_mov_b64 exec, s[22:23]
	v_cmp_lt_u32_e32 vcc, 7, v8
	s_cbranch_vccz .Lp2_c1_p1done
	s_and_saveexec_b64 s[22:23], vcc
	v_bfe_u32 v13, v35, 16, 7
	v_lshlrev_b32_e32 v13, 2, v13
	ds_add_rtn_u32 v75, v13, v12
	s_mov_b64 exec, s[22:23]
.Lp2_c1_p1done:
	s_waitcnt lgkmcnt(7)
	v_cmp_lt_u32_e32 vcc, 0, v9
	s_cbranch_vccz .Lp2_c2_p1done
	s_and_saveexec_b64 s[22:23], vcc
	v_bfe_u32 v13, v36, 16, 7
	v_lshlrev_b32_e32 v13, 2, v13
	ds_add_rtn_u32 v76, v13, v12
	s_mov_b64 exec, s[22:23]
	v_cmp_lt_u32_e32 vcc, 1, v9
	s_cbranch_vccz .Lp2_c2_p1done
	s_and_saveexec_b64 s[22:23], vcc
	v_bfe_u32 v13, v37, 16, 7
	v_lshlrev_b32_e32 v13, 2, v13
	ds_add_rtn_u32 v77, v13, v12
	s_mov_b64 exec, s[22:23]
	v_cmp_lt_u32_e32 vcc, 2, v9
	s_cbranch_vccz .Lp2_c2_p1done
	s_and_saveexec_b64 s[22:23], vcc
	v_bfe_u32 v13, v38, 16, 7
	v_lshlrev_b32_e32 v13, 2, v13
	ds_add_rtn_u32 v78, v13, v12
	s_mov_b64 exec, s[22:23]
	v_cmp_lt_u32_e32 vcc, 3, v9
	s_cbranch_vccz .Lp2_c2_p1done
	s_and_saveexec_b64 s[22:23], vcc
	v_bfe_u32 v13, v39, 16, 7
	v_lshlrev_b32_e32 v13, 2, v13
	ds_add_rtn_u32 v79, v13, v12
	s_mov_b64 exec, s[22:23]
	v_cmp_lt_u32_e32 vcc, 4, v9
	s_cbranch_vccz .Lp2_c2_p1done
	s_and_saveexec_b64 s[22:23], vcc
	v_bfe_u32 v13, v40, 16, 7
	v_lshlrev_b32_e32 v13, 2, v13
	ds_add_rtn_u32 v80, v13, v12
	s_mov_b64 exec, s[22:23]
	v_cmp_lt_u32_e32 vcc, 5, v9
	s_cbranch_vccz .Lp2_c2_p1done
	s_and_saveexec_b64 s[22:23], vcc
	v_bfe_u32 v13, v41, 16, 7
	v_lshlrev_b32_e32 v13, 2, v13
	ds_add_rtn_u32 v81, v13, v12
	s_mov_b64 exec, s[22:23]
	v_cmp_lt_u32_e32 vcc, 6, v9
	s_cbranch_vccz .Lp2_c2_p1done
	s_and_saveexec_b64 s[22:23], vcc
	v_bfe_u32 v13, v42, 16, 7
	v_lshlrev_b32_e32 v13, 2, v13
	ds_add_rtn_u32 v82, v13, v12
	s_mov_b64 exec, s[22:23]
	v_cmp_lt_u32_e32 vcc, 7, v9
	s_cbranch_vccz .Lp2_c2_p1done
	s_and_saveexec_b64 s[22:23], vcc
	v_bfe_u32 v13, v43, 16, 7
	v_lshlrev_b32_e32 v13, 2, v13
	ds_add_rtn_u32 v83, v13, v12
	s_mov_b64 exec, s[22:23]
.Lp2_c2_p1done:
	s_waitcnt lgkmcnt(7)
	v_cmp_lt_u32_e32 vcc, 0, v10
	s_cbranch_vccz .Lp2_c3_p1done
	s_and_saveexec_b64 s[22:23], vcc
	v_bfe_u32 v13, v44, 16, 7
	v_lshlrev_b32_e32 v13, 2, v13
	ds_add_rtn_u32 v84, v13, v12
	s_mov_b64 exec, s[22:23]
	v_cmp_lt_u32_e32 vcc, 1, v10
	s_cbranch_vccz .Lp2_c3_p1done
	s_and_saveexec_b64 s[22:23], vcc
	v_bfe_u32 v13, v45, 16, 7
	v_lshlrev_b32_e32 v13, 2, v13
	ds_add_rtn_u32 v85, v13, v12
	s_mov_b64 exec, s[22:23]
	v_cmp_lt_u32_e32 vcc, 2, v10
	s_cbranch_vccz .Lp2_c3_p1done
	s_and_saveexec_b64 s[22:23], vcc
	v_bfe_u32 v13, v46, 16, 7
	v_lshlrev_b32_e32 v13, 2, v13
	ds_add_rtn_u32 v86, v13, v12
	s_mov_b64 exec, s[22:23]
	v_cmp_lt_u32_e32 vcc, 3, v10
	s_cbranch_vccz .Lp2_c3_p1done
	s_and_saveexec_b64 s[22:23], vcc
	v_bfe_u32 v13, v47, 16, 7
	v_lshlrev_b32_e32 v13, 2, v13
	ds_add_rtn_u32 v87, v13, v12
	s_mov_b64 exec, s[22:23]
	v_cmp_lt_u32_e32 vcc, 4, v10
	s_cbranch_vccz .Lp2_c3_p1done
	s_and_saveexec_b64 s[22:23], vcc
	v_bfe_u32 v13, v48, 16, 7
	v_lshlrev_b32_e32 v13, 2, v13
	ds_add_rtn_u32 v88, v13, v12
	s_mov_b64 exec, s[22:23]
	v_cmp_lt_u32_e32 vcc, 5, v10
	s_cbranch_vccz .Lp2_c3_p1done
	s_and_saveexec_b64 s[22:23], vcc
	v_bfe_u32 v13, v49, 16, 7
	v_lshlrev_b32_e32 v13, 2, v13
	ds_add_rtn_u32 v89, v13, v12
	s_mov_b64 exec, s[22:23]
	v_cmp_lt_u32_e32 vcc, 6, v10
	s_cbranch_vccz .Lp2_c3_p1done
	s_and_saveexec_b64 s[22:23], vcc
	v_bfe_u32 v13, v50, 16, 7
	v_lshlrev_b32_e32 v13, 2, v13
	ds_add_rtn_u32 v90, v13, v12
	s_mov_b64 exec, s[22:23]
	v_cmp_lt_u32_e32 vcc, 7, v10
	s_cbranch_vccz .Lp2_c3_p1done
	s_and_saveexec_b64 s[22:23], vcc
	v_bfe_u32 v13, v51, 16, 7
	v_lshlrev_b32_e32 v13, 2, v13
	ds_add_rtn_u32 v91, v13, v12
	s_mov_b64 exec, s[22:23]
.Lp2_c3_p1done:
	s_waitcnt lgkmcnt(0)
	v_cmp_lt_u32_e32 vcc, 0, v7
	s_cbranch_vccz .Lp2_c0_p2done
	s_and_saveexec_b64 s[22:23], vcc
	v_cmp_gt_u32_e32 vcc, 32, v60
	s_andn2_b64 s[36:37], exec, vcc
	s_or_b64 s[38:39], s[38:39], s[36:37]
	s_and_b64 exec, exec, vcc
	v_lshrrev_b32_e32 v13, 16, v20
	v_lshl_add_u32 v13, v13, 5, v60
	v_lshlrev_b32_e32 v13, 2, v13
	v_and_b32_e32 v14, 0xffff, v20
	global_store_dword v13, v14, s[6:7] nt
	s_mov_b64 exec, s[22:23]
	v_cmp_lt_u32_e32 vcc, 1, v7
	s_cbranch_vccz .Lp2_c0_p2done
	s_and_saveexec_b64 s[22:23], vcc
	v_cmp_gt_u32_e32 vcc, 32, v61
	s_andn2_b64 s[36:37], exec, vcc
	s_or_b64 s[38:39], s[38:39], s[36:37]
	s_and_b64 exec, exec, vcc
	v_lshrrev_b32_e32 v13, 16, v21
	v_lshl_add_u32 v13, v13, 5, v61
	v_lshlrev_b32_e32 v13, 2, v13
	v_and_b32_e32 v14, 0xffff, v21
	global_store_dword v13, v14, s[6:7] nt
	s_mov_b64 exec, s[22:23]
	v_cmp_lt_u32_e32 vcc, 2, v7
	s_cbranch_vccz .Lp2_c0_p2done
	s_and_saveexec_b64 s[22:23], vcc
	v_cmp_gt_u32_e32 vcc, 32, v62
	s_andn2_b64 s[36:37], exec, vcc
	s_or_b64 s[38:39], s[38:39], s[36:37]
	s_and_b64 exec, exec, vcc
	v_lshrrev_b32_e32 v13, 16, v22
	v_lshl_add_u32 v13, v13, 5, v62
	v_lshlrev_b32_e32 v13, 2, v13
	v_and_b32_e32 v14, 0xffff, v22
	global_store_dword v13, v14, s[6:7] nt
	s_mov_b64 exec, s[22:23]
	v_cmp_lt_u32_e32 vcc, 3, v7
	s_cbranch_vccz .Lp2_c0_p2done
	s_and_saveexec_b64 s[22:23], vcc
	v_cmp_gt_u32_e32 vcc, 32, v63
	s_andn2_b64 s[36:37], exec, vcc
	s_or_b64 s[38:39], s[38:39], s[36:37]
	s_and_b64 exec, exec, vcc
	v_lshrrev_b32_e32 v13, 16, v23
	v_lshl_add_u32 v13, v13, 5, v63
	v_lshlrev_b32_e32 v13, 2, v13
	v_and_b32_e32 v14, 0xffff, v23
	global_store_dword v13, v14, s[6:7] nt
	s_mov_b64 exec, s[22:23]
	v_cmp_lt_u32_e32 vcc, 4, v7
	s_cbranch_vccz .Lp2_c0_p2done
	s_and_saveexec_b64 s[22:23], vcc
	v_cmp_gt_u32_e32 vcc, 32, v64
	s_andn2_b64 s[36:37], exec, vcc
	s_or_b64 s[38:39], s[38:39], s[36:37]
	s_and_b64 exec, exec, vcc
	v_lshrrev_b32_e32 v13, 16, v24
	v_lshl_add_u32 v13, v13, 5, v64
	v_lshlrev_b32_e32 v13, 2, v13
	v_and_b32_e32 v14, 0xffff, v24
	global_store_dword v13, v14, s[6:7] nt
	s_mov_b64 exec, s[22:23]
	v_cmp_lt_u32_e32 vcc, 5, v7
	s_cbranch_vccz .Lp2_c0_p2done
	s_and_saveexec_b64 s[22:23], vcc
	v_cmp_gt_u32_e32 vcc, 32, v65
	s_andn2_b64 s[36:37], exec, vcc
	s_or_b64 s[38:39], s[38:39], s[36:37]
	s_and_b64 exec, exec, vcc
	v_lshrrev_b32_e32 v13, 16, v25
	v_lshl_add_u32 v13, v13, 5, v65
	v_lshlrev_b32_e32 v13, 2, v13
	v_and_b32_e32 v14, 0xffff, v25
	global_store_dword v13, v14, s[6:7] nt
	s_mov_b64 exec, s[22:23]
	v_cmp_lt_u32_e32 vcc, 6, v7
	s_cbranch_vccz .Lp2_c0_p2done
	s_and_saveexec_b64 s[22:23], vcc
	v_cmp_gt_u32_e32 vcc, 32, v66
	s_andn2_b64 s[36:37], exec, vcc
	s_or_b64 s[38:39], s[38:39], s[36:37]
	s_and_b64 exec, exec, vcc
	v_lshrrev_b32_e32 v13, 16, v26
	v_lshl_add_u32 v13, v13, 5, v66
	v_lshlrev_b32_e32 v13, 2, v13
	v_and_b32_e32 v14, 0xffff, v26
	global_store_dword v13, v14, s[6:7] nt
	s_mov_b64 exec, s[22:23]
	v_cmp_lt_u32_e32 vcc, 7, v7
	s_cbranch_vccz .Lp2_c0_p2done
	s_and_saveexec_b64 s[22:23], vcc
	v_cmp_gt_u32_e32 vcc, 32, v67
	s_andn2_b64 s[36:37], exec, vcc
	s_or_b64 s[38:39], s[38:39], s[36:37]
	s_and_b64 exec, exec, vcc
	v_lshrrev_b32_e32 v13, 16, v27
	v_lshl_add_u32 v13, v13, 5, v67
	v_lshlrev_b32_e32 v13, 2, v13
	v_and_b32_e32 v14, 0xffff, v27
	global_store_dword v13, v14, s[6:7] nt
	s_mov_b64 exec, s[22:23]
.Lp2_c0_p2done:
	v_cmp_lt_u32_e32 vcc, 0, v8
	s_cbranch_vccz .Lp2_c1_p2done
	s_and_saveexec_b64 s[22:23], vcc
	v_cmp_gt_u32_e32 vcc, 32, v68
	s_andn2_b64 s[36:37], exec, vcc
	s_or_b64 s[38:39], s[38:39], s[36:37]
	s_and_b64 exec, exec, vcc
	v_lshrrev_b32_e32 v13, 16, v28
	v_lshl_add_u32 v13, v13, 5, v68
	v_lshlrev_b32_e32 v13, 2, v13
	v_and_b32_e32 v14, 0xffff, v28
	global_store_dword v13, v14, s[6:7] nt
	s_mov_b64 exec, s[22:23]
	v_cmp_lt_u32_e32 vcc, 1, v8
	s_cbranch_vccz .Lp2_c1_p2done
	s_and_saveexec_b64 s[22:23], vcc
	v_cmp_gt_u32_e32 vcc, 32, v69
	s_andn2_b64 s[36:37], exec, vcc
	s_or_b64 s[38:39], s[38:39], s[36:37]
	s_and_b64 exec, exec, vcc
	v_lshrrev_b32_e32 v13, 16, v29
	v_lshl_add_u32 v13, v13, 5, v69
	v_lshlrev_b32_e32 v13, 2, v13
	v_and_b32_e32 v14, 0xffff, v29
	global_store_dword v13, v14, s[6:7] nt
	s_mov_b64 exec, s[22:23]
	v_cmp_lt_u32_e32 vcc, 2, v8
	s_cbranch_vccz .Lp2_c1_p2done
	s_and_saveexec_b64 s[22:23], vcc
	v_cmp_gt_u32_e32 vcc, 32, v70
	s_andn2_b64 s[36:37], exec, vcc
	s_or_b64 s[38:39], s[38:39], s[36:37]
	s_and_b64 exec, exec, vcc
	v_lshrrev_b32_e32 v13, 16, v30
	v_lshl_add_u32 v13, v13, 5, v70
	v_lshlrev_b32_e32 v13, 2, v13
	v_and_b32_e32 v14, 0xffff, v30
	global_store_dword v13, v14, s[6:7] nt
	s_mov_b64 exec, s[22:23]
	v_cmp_lt_u32_e32 vcc, 3, v8
	s_cbranch_vccz .Lp2_c1_p2done
	s_and_saveexec_b64 s[22:23], vcc
	v_cmp_gt_u32_e32 vcc, 32, v71
	s_andn2_b64 s[36:37], exec, vcc
	s_or_b64 s[38:39], s[38:39], s[36:37]
	s_and_b64 exec, exec, vcc
	v_lshrrev_b32_e32 v13, 16, v31
	v_lshl_add_u32 v13, v13, 5, v71
	v_lshlrev_b32_e32 v13, 2, v13
	v_and_b32_e32 v14, 0xffff, v31
	global_store_dword v13, v14, s[6:7] nt
	s_mov_b64 exec, s[22:23]
	v_cmp_lt_u32_e32 vcc, 4, v8
	s_cbranch_vccz .Lp2_c1_p2done
	s_and_saveexec_b64 s[22:23], vcc
	v_cmp_gt_u32_e32 vcc, 32, v72
	s_andn2_b64 s[36:37], exec, vcc
	s_or_b64 s[38:39], s[38:39], s[36:37]
	s_and_b64 exec, exec, vcc
	v_lshrrev_b32_e32 v13, 16, v32
	v_lshl_add_u32 v13, v13, 5, v72
	v_lshlrev_b32_e32 v13, 2, v13
	v_and_b32_e32 v14, 0xffff, v32
	global_store_dword v13, v14, s[6:7] nt
	s_mov_b64 exec, s[22:23]
	v_cmp_lt_u32_e32 vcc, 5, v8
	s_cbranch_vccz .Lp2_c1_p2done
	s_and_saveexec_b64 s[22:23], vcc
	v_cmp_gt_u32_e32 vcc, 32, v73
	s_andn2_b64 s[36:37], exec, vcc
	s_or_b64 s[38:39], s[38:39], s[36:37]
	s_and_b64 exec, exec, vcc
	v_lshrrev_b32_e32 v13, 16, v33
	v_lshl_add_u32 v13, v13, 5, v73
	v_lshlrev_b32_e32 v13, 2, v13
	v_and_b32_e32 v14, 0xffff, v33
	global_store_dword v13, v14, s[6:7] nt
	s_mov_b64 exec, s[22:23]
	v_cmp_lt_u32_e32 vcc, 6, v8
	s_cbranch_vccz .Lp2_c1_p2done
	s_and_saveexec_b64 s[22:23], vcc
	v_cmp_gt_u32_e32 vcc, 32, v74
	s_andn2_b64 s[36:37], exec, vcc
	s_or_b64 s[38:39], s[38:39], s[36:37]
	s_and_b64 exec, exec, vcc
	v_lshrrev_b32_e32 v13, 16, v34
	v_lshl_add_u32 v13, v13, 5, v74
	v_lshlrev_b32_e32 v13, 2, v13
	v_and_b32_e32 v14, 0xffff, v34
	global_store_dword v13, v14, s[6:7] nt
	s_mov_b64 exec, s[22:23]
	v_cmp_lt_u32_e32 vcc, 7, v8
	s_cbranch_vccz .Lp2_c1_p2done
	s_and_saveexec_b64 s[22:23], vcc
	v_cmp_gt_u32_e32 vcc, 32, v75
	s_andn2_b64 s[36:37], exec, vcc
	s_or_b64 s[38:39], s[38:39], s[36:37]
	s_and_b64 exec, exec, vcc
	v_lshrrev_b32_e32 v13, 16, v35
	v_lshl_add_u32 v13, v13, 5, v75
	v_lshlrev_b32_e32 v13, 2, v13
	v_and_b32_e32 v14, 0xffff, v35
	global_store_dword v13, v14, s[6:7] nt
	s_mov_b64 exec, s[22:23]
.Lp2_c1_p2done:
	v_cmp_lt_u32_e32 vcc, 0, v9
	s_cbranch_vccz .Lp2_c2_p2done
	s_and_saveexec_b64 s[22:23], vcc
	v_cmp_gt_u32_e32 vcc, 32, v76
	s_andn2_b64 s[36:37], exec, vcc
	s_or_b64 s[38:39], s[38:39], s[36:37]
	s_and_b64 exec, exec, vcc
	v_lshrrev_b32_e32 v13, 16, v36
	v_lshl_add_u32 v13, v13, 5, v76
	v_lshlrev_b32_e32 v13, 2, v13
	v_and_b32_e32 v14, 0xffff, v36
	global_store_dword v13, v14, s[6:7] nt
	s_mov_b64 exec, s[22:23]
	v_cmp_lt_u32_e32 vcc, 1, v9
	s_cbranch_vccz .Lp2_c2_p2done
	s_and_saveexec_b64 s[22:23], vcc
	v_cmp_gt_u32_e32 vcc, 32, v77
	s_andn2_b64 s[36:37], exec, vcc
	s_or_b64 s[38:39], s[38:39], s[36:37]
	s_and_b64 exec, exec, vcc
	v_lshrrev_b32_e32 v13, 16, v37
	v_lshl_add_u32 v13, v13, 5, v77
	v_lshlrev_b32_e32 v13, 2, v13
	v_and_b32_e32 v14, 0xffff, v37
	global_store_dword v13, v14, s[6:7] nt
	s_mov_b64 exec, s[22:23]
	v_cmp_lt_u32_e32 vcc, 2, v9
	s_cbranch_vccz .Lp2_c2_p2done
	s_and_saveexec_b64 s[22:23], vcc
	v_cmp_gt_u32_e32 vcc, 32, v78
	s_andn2_b64 s[36:37], exec, vcc
	s_or_b64 s[38:39], s[38:39], s[36:37]
	s_and_b64 exec, exec, vcc
	v_lshrrev_b32_e32 v13, 16, v38
	v_lshl_add_u32 v13, v13, 5, v78
	v_lshlrev_b32_e32 v13, 2, v13
	v_and_b32_e32 v14, 0xffff, v38
	global_store_dword v13, v14, s[6:7] nt
	s_mov_b64 exec, s[22:23]
	v_cmp_lt_u32_e32 vcc, 3, v9
	s_cbranch_vccz .Lp2_c2_p2done
	s_and_saveexec_b64 s[22:23], vcc
	v_cmp_gt_u32_e32 vcc, 32, v79
	s_andn2_b64 s[36:37], exec, vcc
	s_or_b64 s[38:39], s[38:39], s[36:37]
	s_and_b64 exec, exec, vcc
	v_lshrrev_b32_e32 v13, 16, v39
	v_lshl_add_u32 v13, v13, 5, v79
	v_lshlrev_b32_e32 v13, 2, v13
	v_and_b32_e32 v14, 0xffff, v39
	global_store_dword v13, v14, s[6:7] nt
	s_mov_b64 exec, s[22:23]
	v_cmp_lt_u32_e32 vcc, 4, v9
	s_cbranch_vccz .Lp2_c2_p2done
	s_and_saveexec_b64 s[22:23], vcc
	v_cmp_gt_u32_e32 vcc, 32, v80
	s_andn2_b64 s[36:37], exec, vcc
	s_or_b64 s[38:39], s[38:39], s[36:37]
	s_and_b64 exec, exec, vcc
	v_lshrrev_b32_e32 v13, 16, v40
	v_lshl_add_u32 v13, v13, 5, v80
	v_lshlrev_b32_e32 v13, 2, v13
	v_and_b32_e32 v14, 0xffff, v40
	global_store_dword v13, v14, s[6:7] nt
	s_mov_b64 exec, s[22:23]
	v_cmp_lt_u32_e32 vcc, 5, v9
	s_cbranch_vccz .Lp2_c2_p2done
	s_and_saveexec_b64 s[22:23], vcc
	v_cmp_gt_u32_e32 vcc, 32, v81
	s_andn2_b64 s[36:37], exec, vcc
	s_or_b64 s[38:39], s[38:39], s[36:37]
	s_and_b64 exec, exec, vcc
	v_lshrrev_b32_e32 v13, 16, v41
	v_lshl_add_u32 v13, v13, 5, v81
	v_lshlrev_b32_e32 v13, 2, v13
	v_and_b32_e32 v14, 0xffff, v41
	global_store_dword v13, v14, s[6:7] nt
	s_mov_b64 exec, s[22:23]
	v_cmp_lt_u32_e32 vcc, 6, v9
	s_cbranch_vccz .Lp2_c2_p2done
	s_and_saveexec_b64 s[22:23], vcc
	v_cmp_gt_u32_e32 vcc, 32, v82
	s_andn2_b64 s[36:37], exec, vcc
	s_or_b64 s[38:39], s[38:39], s[36:37]
	s_and_b64 exec, exec, vcc
	v_lshrrev_b32_e32 v13, 16, v42
	v_lshl_add_u32 v13, v13, 5, v82
	v_lshlrev_b32_e32 v13, 2, v13
	v_and_b32_e32 v14, 0xffff, v42
	global_store_dword v13, v14, s[6:7] nt
	s_mov_b64 exec, s[22:23]
	v_cmp_lt_u32_e32 vcc, 7, v9
	s_cbranch_vccz .Lp2_c2_p2done
	s_and_saveexec_b64 s[22:23], vcc
	v_cmp_gt_u32_e32 vcc, 32, v83
	s_andn2_b64 s[36:37], exec, vcc
	s_or_b64 s[38:39], s[38:39], s[36:37]
	s_and_b64 exec, exec, vcc
	v_lshrrev_b32_e32 v13, 16, v43
	v_lshl_add_u32 v13, v13, 5, v83
	v_lshlrev_b32_e32 v13, 2, v13
	v_and_b32_e32 v14, 0xffff, v43
	global_store_dword v13, v14, s[6:7] nt
	s_mov_b64 exec, s[22:23]
.Lp2_c2_p2done:
	v_cmp_lt_u32_e32 vcc, 0, v10
	s_cbranch_vccz .Lp2_c3_p2done
	s_and_saveexec_b64 s[22:23], vcc
	v_cmp_gt_u32_e32 vcc, 32, v84
	s_andn2_b64 s[36:37], exec, vcc
	s_or_b64 s[38:39], s[38:39], s[36:37]
	s_and_b64 exec, exec, vcc
	v_lshrrev_b32_e32 v13, 16, v44
	v_lshl_add_u32 v13, v13, 5, v84
	v_lshlrev_b32_e32 v13, 2, v13
	v_and_b32_e32 v14, 0xffff, v44
	global_store_dword v13, v14, s[6:7] nt
	s_mov_b64 exec, s[22:23]
	v_cmp_lt_u32_e32 vcc, 1, v10
	s_cbranch_vccz .Lp2_c3_p2done
	s_and_saveexec_b64 s[22:23], vcc
	v_cmp_gt_u32_e32 vcc, 32, v85
	s_andn2_b64 s[36:37], exec, vcc
	s_or_b64 s[38:39], s[38:39], s[36:37]
	s_and_b64 exec, exec, vcc
	v_lshrrev_b32_e32 v13, 16, v45
	v_lshl_add_u32 v13, v13, 5, v85
	v_lshlrev_b32_e32 v13, 2, v13
	v_and_b32_e32 v14, 0xffff, v45
	global_store_dword v13, v14, s[6:7] nt
	s_mov_b64 exec, s[22:23]
	v_cmp_lt_u32_e32 vcc, 2, v10
	s_cbranch_vccz .Lp2_c3_p2done
	s_and_saveexec_b64 s[22:23], vcc
	v_cmp_gt_u32_e32 vcc, 32, v86
	s_andn2_b64 s[36:37], exec, vcc
	s_or_b64 s[38:39], s[38:39], s[36:37]
	s_and_b64 exec, exec, vcc
	v_lshrrev_b32_e32 v13, 16, v46
	v_lshl_add_u32 v13, v13, 5, v86
	v_lshlrev_b32_e32 v13, 2, v13
	v_and_b32_e32 v14, 0xffff, v46
	global_store_dword v13, v14, s[6:7] nt
	s_mov_b64 exec, s[22:23]
	v_cmp_lt_u32_e32 vcc, 3, v10
	s_cbranch_vccz .Lp2_c3_p2done
	s_and_saveexec_b64 s[22:23], vcc
	v_cmp_gt_u32_e32 vcc, 32, v87
	s_andn2_b64 s[36:37], exec, vcc
	s_or_b64 s[38:39], s[38:39], s[36:37]
	s_and_b64 exec, exec, vcc
	v_lshrrev_b32_e32 v13, 16, v47
	v_lshl_add_u32 v13, v13, 5, v87
	v_lshlrev_b32_e32 v13, 2, v13
	v_and_b32_e32 v14, 0xffff, v47
	global_store_dword v13, v14, s[6:7] nt
	s_mov_b64 exec, s[22:23]
	v_cmp_lt_u32_e32 vcc, 4, v10
	s_cbranch_vccz .Lp2_c3_p2done
	s_and_saveexec_b64 s[22:23], vcc
	v_cmp_gt_u32_e32 vcc, 32, v88
	s_andn2_b64 s[36:37], exec, vcc
	s_or_b64 s[38:39], s[38:39], s[36:37]
	s_and_b64 exec, exec, vcc
	v_lshrrev_b32_e32 v13, 16, v48
	v_lshl_add_u32 v13, v13, 5, v88
	v_lshlrev_b32_e32 v13, 2, v13
	v_and_b32_e32 v14, 0xffff, v48
	global_store_dword v13, v14, s[6:7] nt
	s_mov_b64 exec, s[22:23]
	v_cmp_lt_u32_e32 vcc, 5, v10
	s_cbranch_vccz .Lp2_c3_p2done
	s_and_saveexec_b64 s[22:23], vcc
	v_cmp_gt_u32_e32 vcc, 32, v89
	s_andn2_b64 s[36:37], exec, vcc
	s_or_b64 s[38:39], s[38:39], s[36:37]
	s_and_b64 exec, exec, vcc
	v_lshrrev_b32_e32 v13, 16, v49
	v_lshl_add_u32 v13, v13, 5, v89
	v_lshlrev_b32_e32 v13, 2, v13
	v_and_b32_e32 v14, 0xffff, v49
	global_store_dword v13, v14, s[6:7] nt
	s_mov_b64 exec, s[22:23]
	v_cmp_lt_u32_e32 vcc, 6, v10
	s_cbranch_vccz .Lp2_c3_p2done
	s_and_saveexec_b64 s[22:23], vcc
	v_cmp_gt_u32_e32 vcc, 32, v90
	s_andn2_b64 s[36:37], exec, vcc
	s_or_b64 s[38:39], s[38:39], s[36:37]
	s_and_b64 exec, exec, vcc
	v_lshrrev_b32_e32 v13, 16, v50
	v_lshl_add_u32 v13, v13, 5, v90
	v_lshlrev_b32_e32 v13, 2, v13
	v_and_b32_e32 v14, 0xffff, v50
	global_store_dword v13, v14, s[6:7] nt
	s_mov_b64 exec, s[22:23]
	v_cmp_lt_u32_e32 vcc, 7, v10
	s_cbranch_vccz .Lp2_c3_p2done
	s_and_saveexec_b64 s[22:23], vcc
	v_cmp_gt_u32_e32 vcc, 32, v91
	s_andn2_b64 s[36:37], exec, vcc
	s_or_b64 s[38:39], s[38:39], s[36:37]
	s_and_b64 exec, exec, vcc
	v_lshrrev_b32_e32 v13, 16, v51
	v_lshl_add_u32 v13, v13, 5, v91
	v_lshlrev_b32_e32 v13, 2, v13
	v_and_b32_e32 v14, 0xffff, v51
	global_store_dword v13, v14, s[6:7] nt
	s_mov_b64 exec, s[22:23]
.Lp2_c3_p2done:
	v_cmp_lt_u32_e32 vcc, 0, v11
	s_cbranch_vccz .Lp2_c4_p1done
	s_and_saveexec_b64 s[22:23], vcc
	v_bfe_u32 v13, v52, 16, 7
	v_lshlrev_b32_e32 v13, 2, v13
	ds_add_rtn_u32 v60, v13, v12
	s_mov_b64 exec, s[22:23]
	v_cmp_lt_u32_e32 vcc, 1, v11
	s_cbranch_vccz .Lp2_c4_p1done
	s_and_saveexec_b64 s[22:23], vcc
	v_bfe_u32 v13, v53, 16, 7
	v_lshlrev_b32_e32 v13, 2, v13
	ds_add_rtn_u32 v61, v13, v12
	s_mov_b64 exec, s[22:23]
	v_cmp_lt_u32_e32 vcc, 2, v11
	s_cbranch_vccz .Lp2_c4_p1done
	s_and_saveexec_b64 s[22:23], vcc
	v_bfe_u32 v13, v54, 16, 7
	v_lshlrev_b32_e32 v13, 2, v13
	ds_add_rtn_u32 v62, v13, v12
	s_mov_b64 exec, s[22:23]
	v_cmp_lt_u32_e32 vcc, 3, v11
	s_cbranch_vccz .Lp2_c4_p1done
	s_and_saveexec_b64 s[22:23], vcc
	v_bfe_u32 v13, v55, 16, 7
	v_lshlrev_b32_e32 v13, 2, v13
	ds_add_rtn_u32 v63, v13, v12
	s_mov_b64 exec, s[22:23]
	v_cmp_lt_u32_e32 vcc, 4, v11
	s_cbranch_vccz .Lp2_c4_p1done
	s_and_saveexec_b64 s[22:23], vcc
	v_bfe_u32 v13, v56, 16, 7
	v_lshlrev_b32_e32 v13, 2, v13
	ds_add_rtn_u32 v64, v13, v12
	s_mov_b64 exec, s[22:23]
	v_cmp_lt_u32_e32 vcc, 5, v11
	s_cbranch_vccz .Lp2_c4_p1done
	s_and_saveexec_b64 s[22:23], vcc
	v_bfe_u32 v13, v57, 16, 7
	v_lshlrev_b32_e32 v13, 2, v13
	ds_add_rtn_u32 v65, v13, v12
	s_mov_b64 exec, s[22:23]
	v_cmp_lt_u32_e32 vcc, 6, v11
	s_cbranch_vccz .Lp2_c4_p1done
	s_and_saveexec_b64 s[22:23], vcc
	v_bfe_u32 v13, v58, 16, 7
	v_lshlrev_b32_e32 v13, 2, v13
	ds_add_rtn_u32 v66, v13, v12
	s_mov_b64 exec, s[22:23]
	v_cmp_lt_u32_e32 vcc, 7, v11
	s_cbranch_vccz .Lp2_c4_p1done
	s_and_saveexec_b64 s[22:23], vcc
	v_bfe_u32 v13, v59, 16, 7
	v_lshlrev_b32_e32 v13, 2, v13
	ds_add_rtn_u32 v67, v13, v12
	s_mov_b64 exec, s[22:23]
.Lp2_c4_p1done:
	s_waitcnt lgkmcnt(0)
	v_cmp_lt_u32_e32 vcc, 0, v11
	s_cbranch_vccz .Lp2_c4_p2done
	s_and_saveexec_b64 s[22:23], vcc
	v_cmp_gt_u32_e32 vcc, 32, v60
	s_andn2_b64 s[36:37], exec, vcc
	s_or_b64 s[38:39], s[38:39], s[36:37]
	s_and_b64 exec, exec, vcc
	v_lshrrev_b32_e32 v13, 16, v52
	v_lshl_add_u32 v13, v13, 5, v60
	v_lshlrev_b32_e32 v13, 2, v13
	v_and_b32_e32 v14, 0xffff, v52
	global_store_dword v13, v14, s[6:7] nt
	s_mov_b64 exec, s[22:23]
	v_cmp_lt_u32_e32 vcc, 1, v11
	s_cbranch_vccz .Lp2_c4_p2done
	s_and_saveexec_b64 s[22:23], vcc
	v_cmp_gt_u32_e32 vcc, 32, v61
	s_andn2_b64 s[36:37], exec, vcc
	s_or_b64 s[38:39], s[38:39], s[36:37]
	s_and_b64 exec, exec, vcc
	v_lshrrev_b32_e32 v13, 16, v53
	v_lshl_add_u32 v13, v13, 5, v61
	v_lshlrev_b32_e32 v13, 2, v13
	v_and_b32_e32 v14, 0xffff, v53
	global_store_dword v13, v14, s[6:7] nt
	s_mov_b64 exec, s[22:23]
	v_cmp_lt_u32_e32 vcc, 2, v11
	s_cbranch_vccz .Lp2_c4_p2done
	s_and_saveexec_b64 s[22:23], vcc
	v_cmp_gt_u32_e32 vcc, 32, v62
	s_andn2_b64 s[36:37], exec, vcc
	s_or_b64 s[38:39], s[38:39], s[36:37]
	s_and_b64 exec, exec, vcc
	v_lshrrev_b32_e32 v13, 16, v54
	v_lshl_add_u32 v13, v13, 5, v62
	v_lshlrev_b32_e32 v13, 2, v13
	v_and_b32_e32 v14, 0xffff, v54
	global_store_dword v13, v14, s[6:7] nt
	s_mov_b64 exec, s[22:23]
	v_cmp_lt_u32_e32 vcc, 3, v11
	s_cbranch_vccz .Lp2_c4_p2done
	s_and_saveexec_b64 s[22:23], vcc
	v_cmp_gt_u32_e32 vcc, 32, v63
	s_andn2_b64 s[36:37], exec, vcc
	s_or_b64 s[38:39], s[38:39], s[36:37]
	s_and_b64 exec, exec, vcc
	v_lshrrev_b32_e32 v13, 16, v55
	v_lshl_add_u32 v13, v13, 5, v63
	v_lshlrev_b32_e32 v13, 2, v13
	v_and_b32_e32 v14, 0xffff, v55
	global_store_dword v13, v14, s[6:7] nt
	s_mov_b64 exec, s[22:23]
	v_cmp_lt_u32_e32 vcc, 4, v11
	s_cbranch_vccz .Lp2_c4_p2done
	s_and_saveexec_b64 s[22:23], vcc
	v_cmp_gt_u32_e32 vcc, 32, v64
	s_andn2_b64 s[36:37], exec, vcc
	s_or_b64 s[38:39], s[38:39], s[36:37]
	s_and_b64 exec, exec, vcc
	v_lshrrev_b32_e32 v13, 16, v56
	v_lshl_add_u32 v13, v13, 5, v64
	v_lshlrev_b32_e32 v13, 2, v13
	v_and_b32_e32 v14, 0xffff, v56
	global_store_dword v13, v14, s[6:7] nt
	s_mov_b64 exec, s[22:23]
	v_cmp_lt_u32_e32 vcc, 5, v11
	s_cbranch_vccz .Lp2_c4_p2done
	s_and_saveexec_b64 s[22:23], vcc
	v_cmp_gt_u32_e32 vcc, 32, v65
	s_andn2_b64 s[36:37], exec, vcc
	s_or_b64 s[38:39], s[38:39], s[36:37]
	s_and_b64 exec, exec, vcc
	v_lshrrev_b32_e32 v13, 16, v57
	v_lshl_add_u32 v13, v13, 5, v65
	v_lshlrev_b32_e32 v13, 2, v13
	v_and_b32_e32 v14, 0xffff, v57
	global_store_dword v13, v14, s[6:7] nt
	s_mov_b64 exec, s[22:23]
	v_cmp_lt_u32_e32 vcc, 6, v11
	s_cbranch_vccz .Lp2_c4_p2done
	s_and_saveexec_b64 s[22:23], vcc
	v_cmp_gt_u32_e32 vcc, 32, v66
	s_andn2_b64 s[36:37], exec, vcc
	s_or_b64 s[38:39], s[38:39], s[36:37]
	s_and_b64 exec, exec, vcc
	v_lshrrev_b32_e32 v13, 16, v58
	v_lshl_add_u32 v13, v13, 5, v66
	v_lshlrev_b32_e32 v13, 2, v13
	v_and_b32_e32 v14, 0xffff, v58
	global_store_dword v13, v14, s[6:7] nt
	s_mov_b64 exec, s[22:23]
	v_cmp_lt_u32_e32 vcc, 7, v11
	s_cbranch_vccz .Lp2_c4_p2done
	s_and_saveexec_b64 s[22:23], vcc
	v_cmp_gt_u32_e32 vcc, 32, v67
	s_andn2_b64 s[36:37], exec, vcc
	s_or_b64 s[38:39], s[38:39], s[36:37]
	s_and_b64 exec, exec, vcc
	v_lshrrev_b32_e32 v13, 16, v59
	v_lshl_add_u32 v13, v13, 5, v67
	v_lshlrev_b32_e32 v13, 2, v13
	v_and_b32_e32 v14, 0xffff, v59
	global_store_dword v13, v14, s[6:7] nt
	s_mov_b64 exec, s[22:23]
.Lp2_c4_p2done:
	v_cmp_lt_u32_e32 vcc, 8, v7
	s_cbranch_vccz .Lp2_c0_taildone
	v_mov_b32_e32 v15, 8
.Lp2_c0_tail:
	v_cmp_lt_u32_e32 vcc, v15, v7
	s_and_saveexec_b64 s[22:23], vcc
	s_cbranch_execz .Lp2_c0_tailend
	v_lshl_add_u32 v13, v15, 2, v2
	global_load_dword v16, v13, s[26:27] sc1
	s_waitcnt vmcnt(0)
	v_bfe_u32 v13, v16, 16, 7
	v_lshlrev_b32_e32 v13, 2, v13
	ds_add_rtn_u32 v17, v13, v12
	s_waitcnt lgkmcnt(0)
	v_cmp_gt_u32_e32 vcc, 32, v17
	s_andn2_b64 s[36:37], exec, vcc
	s_or_b64 s[38:39], s[38:39], s[36:37]
	s_and_b64 exec, exec, vcc
	v_lshrrev_b32_e32 v13, 16, v16
	v_lshl_add_u32 v13, v13, 5, v17
	v_lshlrev_b32_e32 v13, 2, v13
	v_and_b32_e32 v14, 0xffff, v16
	global_store_dword v13, v14, s[6:7] nt
	s_mov_b64 exec, s[22:23]
	v_add_u32_e32 v15, 1, v15
	s_branch .Lp2_c0_tail

.Lp2_c0_taildone:
	v_cmp_lt_u32_e32 vcc, 8, v8
	s_cbranch_vccz .Lp2_c1_taildone
	v_mov_b32_e32 v15, 8
.Lp2_c1_tail:
	v_cmp_lt_u32_e32 vcc, v15, v8
	s_and_saveexec_b64 s[22:23], vcc
	s_cbranch_execz .Lp2_c1_tailend
	v_lshl_add_u32 v13, v15, 2, v3
	global_load_dword v16, v13, s[26:27] sc1
	s_waitcnt vmcnt(0)
	v_bfe_u32 v13, v16, 16, 7
	v_lshlrev_b32_e32 v13, 2, v13
	ds_add_rtn_u32 v17, v13, v12
	s_waitcnt lgkmcnt(0)
	v_cmp_gt_u32_e32 vcc, 32, v17
	s_andn2_b64 s[36:37], exec, vcc
	s_or_b64 s[38:39], s[38:39], s[36:37]
	s_and_b64 exec, exec, vcc
	v_lshrrev_b32_e32 v13, 16, v16
	v_lshl_add_u32 v13, v13, 5, v17
	v_lshlrev_b32_e32 v13, 2, v13
	v_and_b32_e32 v14, 0xffff, v16
	global_store_dword v13, v14, s[6:7] nt
	s_mov_b64 exec, s[22:23]
	v_add_u32_e32 v15, 1, v15
	s_branch .Lp2_c1_tail

.Lp2_c1_taildone:
	v_cmp_lt_u32_e32 vcc, 8, v9
	s_cbranch_vccz .Lp2_c2_taildone
	v_mov_b32_e32 v15, 8
.Lp2_c2_tail:
	v_cmp_lt_u32_e32 vcc, v15, v9
	s_and_saveexec_b64 s[22:23], vcc
	s_cbranch_execz .Lp2_c2_tailend
	v_lshl_add_u32 v13, v15, 2, v4
	global_load_dword v16, v13, s[26:27] sc1
	s_waitcnt vmcnt(0)
	v_bfe_u32 v13, v16, 16, 7
	v_lshlrev_b32_e32 v13, 2, v13
	ds_add_rtn_u32 v17, v13, v12
	s_waitcnt lgkmcnt(0)
	v_cmp_gt_u32_e32 vcc, 32, v17
	s_andn2_b64 s[36:37], exec, vcc
	s_or_b64 s[38:39], s[38:39], s[36:37]
	s_and_b64 exec, exec, vcc
	v_lshrrev_b32_e32 v13, 16, v16
	v_lshl_add_u32 v13, v13, 5, v17
	v_lshlrev_b32_e32 v13, 2, v13
	v_and_b32_e32 v14, 0xffff, v16
	global_store_dword v13, v14, s[6:7] nt
	s_mov_b64 exec, s[22:23]
	v_add_u32_e32 v15, 1, v15
	s_branch .Lp2_c2_tail

.Lp2_c2_taildone:
	v_cmp_lt_u32_e32 vcc, 8, v10
	s_cbranch_vccz .Lp2_c3_taildone
	v_mov_b32_e32 v15, 8
.Lp2_c3_tail:
	v_cmp_lt_u32_e32 vcc, v15, v10
	s_and_saveexec_b64 s[22:23], vcc
	s_cbranch_execz .Lp2_c3_tailend
	v_lshl_add_u32 v13, v15, 2, v5
	global_load_dword v16, v13, s[26:27] sc1
	s_waitcnt vmcnt(0)
	v_bfe_u32 v13, v16, 16, 7
	v_lshlrev_b32_e32 v13, 2, v13
	ds_add_rtn_u32 v17, v13, v12
	s_waitcnt lgkmcnt(0)
	v_cmp_gt_u32_e32 vcc, 32, v17
	s_andn2_b64 s[36:37], exec, vcc
	s_or_b64 s[38:39], s[38:39], s[36:37]
	s_and_b64 exec, exec, vcc
	v_lshrrev_b32_e32 v13, 16, v16
	v_lshl_add_u32 v13, v13, 5, v17
	v_lshlrev_b32_e32 v13, 2, v13
	v_and_b32_e32 v14, 0xffff, v16
	global_store_dword v13, v14, s[6:7] nt
	s_mov_b64 exec, s[22:23]
	v_add_u32_e32 v15, 1, v15
	s_branch .Lp2_c3_tail

.Lp2_c3_taildone:
	v_cmp_lt_u32_e32 vcc, 8, v11
	s_cbranch_vccz .Lp2_c4_taildone
	v_mov_b32_e32 v15, 8
.Lp2_c4_tail:
	v_cmp_lt_u32_e32 vcc, v15, v11
	s_and_saveexec_b64 s[22:23], vcc
	s_cbranch_execz .Lp2_c4_tailend
	v_lshl_add_u32 v13, v15, 2, v6
	global_load_dword v16, v13, s[26:27] sc1
	s_waitcnt vmcnt(0)
	v_bfe_u32 v13, v16, 16, 7
	v_lshlrev_b32_e32 v13, 2, v13
	ds_add_rtn_u32 v17, v13, v12
	s_waitcnt lgkmcnt(0)
	v_cmp_gt_u32_e32 vcc, 32, v17
	s_andn2_b64 s[36:37], exec, vcc
	s_or_b64 s[38:39], s[38:39], s[36:37]
	s_and_b64 exec, exec, vcc
	v_lshrrev_b32_e32 v13, 16, v16
	v_lshl_add_u32 v13, v13, 5, v17
	v_lshlrev_b32_e32 v13, 2, v13
	v_and_b32_e32 v14, 0xffff, v16
	global_store_dword v13, v14, s[6:7] nt
	s_mov_b64 exec, s[22:23]
	v_add_u32_e32 v15, 1, v15
	s_branch .Lp2_c4_tail

.Lp2_c4_taildone:
	s_cmp_eq_u64 s[38:39], 0
	s_cbranch_scc1 .Lp2_noflag
	ds_write_b32 v19, v12 offset:1028
.Lp2_noflag:
	s_waitcnt lgkmcnt(0)
	s_barrier
	v_lshlrev_b32_e32 v13, 2, v0
	ds_read_b32 v14, v13
	ds_read_b32 v18, v19 offset:1028
	s_lshl_b32 s3, s33, 7
	v_add_u32_e32 v16, s3, v0
	v_lshlrev_b32_e32 v13, 2, v16
	s_waitcnt lgkmcnt(0)
	v_cmp_gt_u32_e32 vcc, s30, v16
	s_mov_b64 s[28:29], -1
	s_and_b64 vcc, vcc, s[28:29]
	s_and_saveexec_b64 s[22:23], vcc
	global_store_dword v13, v14, s[4:5]
	s_mov_b64 exec, s[22:23]
	v_readfirstlane_b32 s3, v18
	s_cmp_eq_u32 s3, 0
	s_cbranch_scc1 .Lp2_end
	s_waitcnt vmcnt(0)
	s_barrier
	v_mov_b32_e32 v15, 0
.Lp2_s0_loop:
	v_cmp_lt_u32_e32 vcc, v15, v7
	s_and_saveexec_b64 s[22:23], vcc
	s_cbranch_execz .Lp2_s0_end
	v_lshl_add_u32 v13, v15, 2, v2
	global_load_dword v16, v13, s[26:27] sc1
	s_waitcnt vmcnt(0)
	v_bfe_u32 v13, v16, 16, 7
	v_lshlrev_b32_e32 v13, 2, v13
	ds_read_b32 v17, v13
	s_waitcnt lgkmcnt(0)
	v_cmp_lt_u32_e32 vcc, 32, v17
	s_and_b64 exec, exec, vcc
	s_cbranch_execz .Lp2_s0_next
	ds_add_rtn_u32 v17, v13, v12 offset:2048
	v_lshrrev_b32_e32 v18, 16, v16
	v_and_b32_e32 v14, 0xffff, v16
	s_waitcnt lgkmcnt(0)
	s_mov_b64 s[28:29], exec
	v_cmp_gt_u32_e32 vcc, 32, v17
	s_and_b64 exec, s[28:29], vcc
	v_lshl_add_u32 v13, v18, 5, v17
	v_lshlrev_b32_e32 v13, 2, v13
	global_store_dword v13, v14, s[6:7]
	s_andn2_b64 exec, s[28:29], vcc
	s_cbranch_execz .Lp2_s0_next
	global_atomic_add v13, v19, v12, s[10:11] sc0
	s_waitcnt vmcnt(0)
	v_lshlrev_b32_e32 v13, 2, v13
	global_store_dword v13, v18, s[16:17]
	global_store_dword v13, v14, s[18:19]
	v_cmp_eq_u32_e32 vcc, 32, v17
	s_and_b64 exec, exec, vcc
	s_cbranch_execz .Lp2_s0_next
	global_atomic_add v13, v19, v12, s[10:11] offset:4 sc0
	s_waitcnt vmcnt(0)
	v_lshlrev_b32_e32 v13, 2, v13
	global_store_dword v13, v18, s[20:21]

.Lp2_s1_loop:
	v_cmp_lt_u32_e32 vcc, v15, v8
	s_and_saveexec_b64 s[22:23], vcc
	s_cbranch_execz .Lp2_s1_end
	v_lshl_add_u32 v13, v15, 2, v3
	global_load_dword v16, v13, s[26:27] sc1
	s_waitcnt vmcnt(0)
	v_bfe_u32 v13, v16, 16, 7
	v_lshlrev_b32_e32 v13, 2, v13
	ds_read_b32 v17, v13
	s_waitcnt lgkmcnt(0)
	v_cmp_lt_u32_e32 vcc, 32, v17
	s_and_b64 exec, exec, vcc
	s_cbranch_execz .Lp2_s1_next
	ds_add_rtn_u32 v17, v13, v12 offset:2048
	v_lshrrev_b32_e32 v18, 16, v16
	v_and_b32_e32 v14, 0xffff, v16
	s_waitcnt lgkmcnt(0)
	s_mov_b64 s[28:29], exec
	v_cmp_gt_u32_e32 vcc, 32, v17
	s_and_b64 exec, s[28:29], vcc
	v_lshl_add_u32 v13, v18, 5, v17
	v_lshlrev_b32_e32 v13, 2, v13
	global_store_dword v13, v14, s[6:7]
	s_andn2_b64 exec, s[28:29], vcc
	s_cbranch_execz .Lp2_s1_next
	global_atomic_add v13, v19, v12, s[10:11] sc0
	s_waitcnt vmcnt(0)
	v_lshlrev_b32_e32 v13, 2, v13
	global_store_dword v13, v18, s[16:17]
	global_store_dword v13, v14, s[18:19]
	v_cmp_eq_u32_e32 vcc, 32, v17
	s_and_b64 exec, exec, vcc
	s_cbranch_execz .Lp2_s1_next
	global_atomic_add v13, v19, v12, s[10:11] offset:4 sc0
	s_waitcnt vmcnt(0)
	v_lshlrev_b32_e32 v13, 2, v13
	global_store_dword v13, v18, s[20:21]

.Lp2_s2_loop:
	v_cmp_lt_u32_e32 vcc, v15, v9
	s_and_saveexec_b64 s[22:23], vcc
	s_cbranch_execz .Lp2_s2_end
	v_lshl_add_u32 v13, v15, 2, v4
	global_load_dword v16, v13, s[26:27] sc1
	s_waitcnt vmcnt(0)
	v_bfe_u32 v13, v16, 16, 7
	v_lshlrev_b32_e32 v13, 2, v13
	ds_read_b32 v17, v13
	s_waitcnt lgkmcnt(0)
	v_cmp_lt_u32_e32 vcc, 32, v17
	s_and_b64 exec, exec, vcc
	s_cbranch_execz .Lp2_s2_next
	ds_add_rtn_u32 v17, v13, v12 offset:2048
	v_lshrrev_b32_e32 v18, 16, v16
	v_and_b32_e32 v14, 0xffff, v16
	s_waitcnt lgkmcnt(0)
	s_mov_b64 s[28:29], exec
	v_cmp_gt_u32_e32 vcc, 32, v17
	s_and_b64 exec, s[28:29], vcc
	v_lshl_add_u32 v13, v18, 5, v17
	v_lshlrev_b32_e32 v13, 2, v13
	global_store_dword v13, v14, s[6:7]
	s_andn2_b64 exec, s[28:29], vcc
	s_cbranch_execz .Lp2_s2_next
	global_atomic_add v13, v19, v12, s[10:11] sc0
	s_waitcnt vmcnt(0)
	v_lshlrev_b32_e32 v13, 2, v13
	global_store_dword v13, v18, s[16:17]
	global_store_dword v13, v14, s[18:19]
	v_cmp_eq_u32_e32 vcc, 32, v17
	s_and_b64 exec, exec, vcc
	s_cbranch_execz .Lp2_s2_next
	global_atomic_add v13, v19, v12, s[10:11] offset:4 sc0
	s_waitcnt vmcnt(0)
	v_lshlrev_b32_e32 v13, 2, v13
	global_store_dword v13, v18, s[20:21]

.Lp2_s3_loop:
	v_cmp_lt_u32_e32 vcc, v15, v10
	s_and_saveexec_b64 s[22:23], vcc
	s_cbranch_execz .Lp2_s3_end
	v_lshl_add_u32 v13, v15, 2, v5
	global_load_dword v16, v13, s[26:27] sc1
	s_waitcnt vmcnt(0)
	v_bfe_u32 v13, v16, 16, 7
	v_lshlrev_b32_e32 v13, 2, v13
	ds_read_b32 v17, v13
	s_waitcnt lgkmcnt(0)
	v_cmp_lt_u32_e32 vcc, 32, v17
	s_and_b64 exec, exec, vcc
	s_cbranch_execz .Lp2_s3_next
	ds_add_rtn_u32 v17, v13, v12 offset:2048
	v_lshrrev_b32_e32 v18, 16, v16
	v_and_b32_e32 v14, 0xffff, v16
	s_waitcnt lgkmcnt(0)
	s_mov_b64 s[28:29], exec
	v_cmp_gt_u32_e32 vcc, 32, v17
	s_and_b64 exec, s[28:29], vcc
	v_lshl_add_u32 v13, v18, 5, v17
	v_lshlrev_b32_e32 v13, 2, v13
	global_store_dword v13, v14, s[6:7]
	s_andn2_b64 exec, s[28:29], vcc
	s_cbranch_execz .Lp2_s3_next
	global_atomic_add v13, v19, v12, s[10:11] sc0
	s_waitcnt vmcnt(0)
	v_lshlrev_b32_e32 v13, 2, v13
	global_store_dword v13, v18, s[16:17]
	global_store_dword v13, v14, s[18:19]
	v_cmp_eq_u32_e32 vcc, 32, v17
	s_and_b64 exec, exec, vcc
	s_cbranch_execz .Lp2_s3_next
	global_atomic_add v13, v19, v12, s[10:11] offset:4 sc0
	s_waitcnt vmcnt(0)
	v_lshlrev_b32_e32 v13, 2, v13
	global_store_dword v13, v18, s[20:21]

.Lp2_s4_loop:
	v_cmp_lt_u32_e32 vcc, v15, v11
	s_and_saveexec_b64 s[22:23], vcc
	s_cbranch_execz .Lp2_s4_end
	v_lshl_add_u32 v13, v15, 2, v6
	global_load_dword v16, v13, s[26:27] sc1
	s_waitcnt vmcnt(0)
	v_bfe_u32 v13, v16, 16, 7
	v_lshlrev_b32_e32 v13, 2, v13
	ds_read_b32 v17, v13
	s_waitcnt lgkmcnt(0)
	v_cmp_lt_u32_e32 vcc, 32, v17
	s_and_b64 exec, exec, vcc
	s_cbranch_execz .Lp2_s4_next
	ds_add_rtn_u32 v17, v13, v12 offset:2048
	v_lshrrev_b32_e32 v18, 16, v16
	v_and_b32_e32 v14, 0xffff, v16
	s_waitcnt lgkmcnt(0)
	s_mov_b64 s[28:29], exec
	v_cmp_gt_u32_e32 vcc, 32, v17
	s_and_b64 exec, s[28:29], vcc
	v_lshl_add_u32 v13, v18, 5, v17
	v_lshlrev_b32_e32 v13, 2, v13
	global_store_dword v13, v14, s[6:7]
	s_andn2_b64 exec, s[28:29], vcc
	s_cbranch_execz .Lp2_s4_next
	global_atomic_add v13, v19, v12, s[10:11] sc0
	s_waitcnt vmcnt(0)
	v_lshlrev_b32_e32 v13, 2, v13
	global_store_dword v13, v18, s[16:17]
	global_store_dword v13, v14, s[18:19]
	v_cmp_eq_u32_e32 vcc, 32, v17
	s_and_b64 exec, exec, vcc
	s_cbranch_execz .Lp2_s4_next
	global_atomic_add v13, v19, v12, s[10:11] offset:4 sc0
	s_waitcnt vmcnt(0)
	v_lshlrev_b32_e32 v13, 2, v13
	global_store_dword v13, v18, s[20:21]

_Z4k_l1PKDF16_PKfPKiS4_S4_S4_S4_S4_S4_S2_S2_S0_S0_S2_S2_S2_PDF16_Pf:
	s_load_dwordx2 s[10:11], s[0:1], 0x80
	s_load_dwordx2 s[36:37], s[0:1], 0x68
	s_load_dwordx4 s[16:19], s[0:1], 0x0
	s_load_dwordx4 s[28:31], s[0:1], 0x18
	v_and_b32_e32 v1, 63, v0
	v_lshrrev_b32_e32 v66, 6, v0
	s_cmpk_lt_u32 s2, 27
	s_cbranch_scc0 .Lmy_l1_noprio
	s_setprio 3
.Lmy_l1_noprio:
	s_cmpk_lt_u32 s2, 0x200
	s_mov_b64 s[4:5], -1
	s_cbranch_scc0 .LBB2_32
	s_load_dwordx2 s[12:13], s[0:1], 0x10
	s_load_dwordx4 s[4:7], s[0:1], 0x58
	s_lshl_b32 s3, s2, 5
	v_lshlrev_b32_e32 v2, 2, v66
	v_lshrrev_b32_e32 v3, 4, v1
	v_or3_b32 v62, v2, s3, v3
	v_mov_b32_e32 v63, 0
	s_waitcnt lgkmcnt(0)
	v_lshl_add_u64 v[2:3], v[62:63], 2, s[12:13]
	global_load_dword v56, v[2:3], off
	v_and_b32_e32 v57, 15, v0
	v_lshlrev_b64 v[2:3], 7, v[62:63]
	v_lshl_add_u64 v[2:3], s[28:29], 0, v[2:3]
	v_lshlrev_b32_e32 v4, 2, v57
	v_mov_b32_e32 v5, v63
	v_lshl_add_u64 v[2:3], v[2:3], 0, v[4:5]
	global_load_dword v64, v[2:3], off
	v_lshlrev_b32_e32 v2, 3, v0
	s_movk_i32 s9, 0x3f00
	v_mov_b32_e32 v4, 0x3000
	v_lshlrev_b32_e32 v5, 8, v0
	s_movk_i32 s3, 0x1f00
	v_mov_b32_e32 v3, 0x1000
	v_bitop3_b32 v12, v2, s9, v4 bitop3:0xc8
	v_and_b32_e32 v13, 0x1f00, v5
	v_lshlrev_b64 v[4:5], 8, v[62:63]
	v_lshlrev_b32_e32 v67, 4, v0
	v_lshlrev_b32_e32 v6, 4, v57
	v_mov_b32_e32 v7, v63
	v_bitop3_b32 v11, v2, s3, v3 bitop3:0xc8
	v_lshlrev_b64 v[2:3], 5, v[62:63]
	v_lshl_add_u64 v[24:25], s[16:17], 0, v[4:5]
	v_lshrrev_b32_e32 v10, 1, v0
	v_and_b32_e32 v8, 0x1f0, v67
	v_mov_b32_e32 v9, v63
	v_lshl_add_u64 v[22:23], s[18:19], 0, v[2:3]
	v_lshl_add_u64 v[6:7], v[24:25], 0, v[6:7]
	v_and_b32_e32 v54, 0x1e00, v67
	v_mov_b32_e32 v55, v63
	v_mov_b32_e32 v19, v63
	v_and_b32_e32 v20, 16, v10
	v_lshlrev_b32_e32 v14, 1, v11
	v_lshlrev_b32_e32 v16, 1, v12
	v_lshl_or_b32 v18, v66, 13, v13
	global_load_dwordx4 v[2:5], v[22:23], off offset:16
	global_load_dwordx4 v[10:13], v[22:23], off
	global_load_dwordx4 v[50:53], v[6:7], off
	v_lshl_add_u64 v[6:7], s[6:7], 0, v[8:9]
	s_movk_i32 s8, 0x4000
	v_lshl_add_u64 v[8:9], s[4:5], 0, v[18:19]
	v_lshl_add_u64 v[18:19], v[6:7], 0, v[54:55]
	v_add_co_u32_e32 v42, vcc, s8, v18
	v_mov_b32_e32 v15, v63
	s_nop 0
	v_addc_co_u32_e32 v43, vcc, 0, v19, vcc
	v_mov_b32_e32 v17, v63
	v_mov_b32_e32 v21, v63
	v_lshl_add_u64 v[22:23], v[6:7], 0, v[14:15]
	v_lshl_add_u64 v[6:7], v[6:7], 0, v[16:17]
	global_load_dwordx4 v[14:17], v[18:19], off
	global_load_dwordx4 v[58:61], v[22:23], off
	v_lshl_add_u64 v[8:9], v[8:9], 0, v[20:21]
	global_load_dwordx4 v[18:21], v[8:9], off
	global_load_dwordx4 v[22:25], v[8:9], off offset:32
	global_load_dwordx4 v[26:29], v[8:9], off offset:64
	global_load_dwordx4 v[30:33], v[8:9], off offset:96
	global_load_dwordx4 v[68:71], v[42:43], off
	global_load_dwordx4 v[34:37], v[8:9], off offset:128
	global_load_dwordx4 v[38:41], v[8:9], off offset:160
	s_nop 0
	global_load_dwordx4 v[42:45], v[8:9], off offset:192
	global_load_dwordx4 v[46:49], v[8:9], off offset:224
	global_load_dwordx4 v[72:75], v[6:7], off
	v_lshrrev_b32_e32 v55, 5, v0
	s_movk_i32 s3, 0x3e00
	s_mov_b32 s14, 0x3e4ccccd
	s_mov_b32 s15, s2
	s_waitcnt vmcnt(16)
	v_cmp_gt_i32_e32 vcc, v56, v57
	v_bitop3_b32 v57, v55, v0, 31 bitop3:0x78
	v_lshlrev_b32_e32 v57, 4, v57
	v_lshl_or_b32 v55, v55, 9, v57
	s_waitcnt vmcnt(15)
	v_cndmask_b32_e32 v64, v62, v64, vcc
	v_ashrrev_i32_e32 v65, 31, v64
	v_lshlrev_b64 v[6:7], 5, v[64:65]
	v_lshl_add_u64 v[6:7], s[18:19], 0, v[6:7]
	global_load_dwordx4 v[6:9], v[6:7], off
	v_mov_b32_e32 v65, 0xc34f
	s_waitcnt vmcnt(12)
	ds_write_b128 v55, v[14:17] offset:49152
	v_or_b32_e32 v14, 0x2000, v67
	v_and_or_b32 v14, v14, s3, v57
	s_mov_b32 s3, 0x10000
	s_waitcnt vmcnt(11)
	ds_write_b128 v14, v[58:61] offset:49152
	v_or3_b32 v14, v54, v57, s3
	s_waitcnt vmcnt(6)
	ds_write_b128 v14, v[68:71]
	v_or_b32_e32 v14, 0x6000, v67
	s_movk_i32 s3, 0x7e00
	v_and_or_b32 v14, v14, s3, v57
	s_mov_b32 s3, 0xc350
	v_mov_b32_e32 v67, 0xff800000
	s_waitcnt vmcnt(1)
	ds_write_b128 v14, v[72:75] offset:49152
	s_branch .LBB2_3

_Z4k_l2PKDF16_PKfPKiS4_S4_S4_S4_S4_S4_S2_S2_S2_PfPi:
	s_cmpk_lt_u32 s2, 53
	s_cbranch_scc0 .Lmy_l2_noprio
	s_setprio 3
.Lmy_l2_noprio:
	s_load_dwordx8 s[12:19], s[0:1], 0x50
	s_load_dwordx8 s[20:27], s[0:1], 0x30
	s_load_dwordx2 s[28:29], s[0:1], 0x0
	s_load_dwordx8 s[36:43], s[0:1], 0x10
	v_lshlrev_b32_e32 v7, 2, v0
	s_mov_b32 s4, 0
	s_mov_b32 s5, 1
	s_mov_b64 s[6:7], 0
	v_mov_b32_e32 v1, 0
	v_mov_b32_e32 v2, v7
	s_mov_b32 s8, s4
	s_branch .LBB3_2
